# route phase: pass-1 row loads hoisted, pass-2 hand-pipelined (depth-4 loads, LDS tables for norm/scale/shift), router-weight bf16 hi/lo table stored in MFMA-fragment order for coalesced loads
# speedup vs baseline: 1.0332x; 1.0175x over previous
.LBB0_32:
	s_cmpk_gt_i32 s75, 0x2f3f
	s_cbranch_scc1 .LBB0_278
	v_readlane_b32 s0, v255, 7
	s_mulk_i32 s0, 0x4100
	s_add_i32 s2, s0, 0
	s_add_u32 s69, s50, 0x39c00000
	s_addc_u32 s72, s51, 0
	s_add_u32 s0, s50, 0x36c00000
	v_writelane_b32 v255, s0, 9
	s_addc_u32 s0, s51, 0
	v_writelane_b32 v255, s0, 10
	s_add_u32 s0, s50, 0x37400000
	v_writelane_b32 v255, s0, 11
	s_addc_u32 s0, s51, 0
	s_waitcnt lgkmcnt(11)
	v_lshlrev_b32_e32 v4, 3, v254
	v_writelane_b32 v255, s0, 13
	s_add_u32 s0, s50, 0x1c200000
	v_mov_b32_e32 v3, 0
	v_and_b32_e32 v16, 56, v4
	v_writelane_b32 v255, s0, 15
	s_addc_u32 s0, s51, 0
	v_lshlrev_b32_e32 v6, 1, v16
	v_mov_b32_e32 v7, v3
	v_and_b32_e32 v40, 31, v0
	v_writelane_b32 v255, s0, 17
	v_lshl_add_u64 v[6:7], s[50:51], 0, v[6:7]
	s_mov_b64 s[0:1], 0x380000
	s_waitcnt lgkmcnt(8)
	v_cvt_f32_ubyte0_e32 v5, v40
	v_lshl_add_u64 v[6:7], v[6:7], 0, s[0:1]
	v_mul_f32_e32 v8, 0xbed49a78, v5
	s_mov_b32 s0, 0xc2fc0000
	s_waitcnt lgkmcnt(7)
	v_mov_b32_e32 v9, 0x42800000
	v_cmp_gt_f32_e32 vcc, s0, v8
	v_not_b32_e32 v45, 63
	s_add_u32 s4, s50, 0x184000
	v_cndmask_b32_e32 v8, 0, v9, vcc
	v_fmac_f32_e32 v8, 0xbed49a78, v5
	v_exp_f32_e32 v5, v8
	v_cndmask_b32_e32 v8, 0, v45, vcc
	s_addc_u32 s5, s51, 0
	v_mov_b32_e32 v9, v3
	v_ldexp_f32 v46, v5, v8
	v_lshlrev_b32_e32 v8, 4, v254
	v_writelane_b32 v255, s4, 19
	v_lshl_add_u64 v[8:9], s[50:51], 0, v[8:9]
	s_mov_b64 s[0:1], 0x3bc00000
	v_writelane_b32 v255, s5, 20
	v_lshl_add_u64 v[8:9], v[8:9], 0, s[0:1]
	s_add_u32 s0, s50, 0x30600000
	v_writelane_b32 v255, s0, 21
	s_addc_u32 s0, s51, 0
	v_lshlrev_b32_e32 v2, 2, v0
	s_add_u32 s84, s50, 0x34800000
	v_lshrrev_b32_e32 v1, 4, v254
	v_and_b32_e32 v2, 60, v2
	v_lshrrev_b32_e32 v44, 3, v254
	s_addc_u32 s85, s51, 0
	s_waitcnt lgkmcnt(5)
	v_lshlrev_b32_e32 v18, 2, v2
	v_mul_u32_u24_e32 v13, 0x104, v16
	v_writelane_b32 v255, s0, 22
	v_mul_u32_u24_e32 v12, 0x104, v1
	v_lshlrev_b32_e32 v14, 2, v44
	s_add_u32 s0, s50, 0x3a400000
	v_lshl_or_b32 v2, v1, 8, v18
	v_lshl_or_b32 v10, v1, 13, v18
	v_add3_u32 v48, s2, v18, v12
	v_add3_u32 v49, s2, v13, v14
	v_lshl_or_b32 v14, v1, 11, v18
	v_lshl_or_b32 v18, v1, 15, v18
	v_writelane_b32 v255, s0, 23
	s_addc_u32 s0, s51, 0
	v_lshrrev_b32_e32 v1, 2, v254
	v_and_b32_e32 v36, 0xf8, v4
	v_writelane_b32 v255, s0, 25
	s_movk_i32 s0, 0x7f
	v_and_b32_e32 v1, 8, v1
	s_lshl_b32 s95, s75, 6
	v_cmp_lt_u32_e64 s[0:1], s0, v36
	v_lshl_add_u64 v[36:37], s[64:65], 0, v[2:3]
	v_sub_u32_e32 v50, v1, v44
	v_or_b32_e32 v1, s95, v254
	v_mov_b32_e32 v2, 0xffe87000
	v_lshl_add_u32 v2, v1, 1, v2
	v_lshlrev_b32_e32 v1, 8, v40
	v_or_b32_e32 v41, 32, v1
	v_mul_lo_u32 v51, s75, v41
	v_mul_lo_u32 v52, s74, v41
	v_or_b32_e32 v41, 64, v1
	v_mul_lo_u32 v53, s75, v41
	v_mul_lo_u32 v54, s74, v41
	v_or_b32_e32 v41, 0x60, v1
	v_mul_lo_u32 v55, s75, v41
	v_mul_lo_u32 v56, s74, v41
	v_or_b32_e32 v41, 0x80, v1
	v_mul_lo_u32 v57, s75, v41
	v_mul_lo_u32 v58, s74, v41
	v_or_b32_e32 v41, 0xa0, v1
	v_mul_lo_u32 v59, s75, v41
	v_mul_lo_u32 v60, s74, v41
	v_or_b32_e32 v41, 0xc0, v1
	v_or_b32_e32 v1, 0xe0, v1
	v_mov_b32_e32 v5, v3
	v_writelane_b32 v255, s0, 26
	v_mul_lo_u32 v63, s75, v1
	v_mul_lo_u32 v64, s74, v1
	v_mul_lo_u32 v1, s75, v40
	v_mov_b32_e32 v20, 0
	v_writelane_b32 v255, s1, 27
	v_lshl_add_u64 v[38:39], s[50:51], 0, v[4:5]
	s_mov_b64 s[0:1], 0x37c00000
	v_lshlrev_b32_e32 v65, 8, v1
	v_mul_lo_u32 v1, s74, v40
	v_lshrrev_b32_e32 v47, 5, v254
	v_mov_b32_e32 v11, v3
	v_lshl_or_b32 v12, v44, 9, v16
	v_mov_b32_e32 v13, v3
	v_mov_b32_e32 v15, v3
	v_lshl_or_b32 v16, v44, 11, v16
	v_mov_b32_e32 v17, v3
	s_waitcnt lgkmcnt(2)
	v_mov_b32_e32 v19, v3
	v_mov_b32_e32 v21, v3
	s_mov_b32 s88, 0x8000
	v_mov_b32_e32 v22, 0x80
	v_mov_b32_e32 v23, v3
	s_mov_b32 s89, 0x10000
	v_mov_b32_e32 v24, 0x100
	v_mov_b32_e32 v25, v3
	s_mov_b32 s90, 0x18000
	v_mov_b32_e32 v26, 0x180
	s_waitcnt lgkmcnt(1)
	v_mov_b32_e32 v27, v3
	s_mov_b32 s91, 0x20000
	v_mov_b32_e32 v28, 0x20000
	v_mov_b32_e32 v29, v3
	v_mov_b32_e32 v30, 0x20080
	s_waitcnt lgkmcnt(0)
	v_mov_b32_e32 v31, v3
	v_mov_b32_e32 v32, 0x20100
	v_mov_b32_e32 v33, v3
	s_mov_b32 s94, 0x38000
	v_mov_b32_e32 v34, 0x20180
	v_mov_b32_e32 v35, v3
	v_lshl_add_u64 v[38:39], v[38:39], 0, s[0:1]
	s_lshl_b32 s96, s74, 6
	s_lshl_b32 s97, s75, 17
	s_lshl_b32 s82, s74, 17
	v_or_b32_e32 v5, 0xfff43800, v254
	s_lshl_b32 s83, s74, 7
	v_mul_lo_u32 v61, s75, v41
	v_mul_lo_u32 v62, s74, v41
	v_lshlrev_b32_e32 v66, 8, v1
	s_lshl_b32 s80, s75, 1
	s_lshl_b32 s81, s74, 1
	s_mov_b32 s1, 0x40000
	s_mov_b32 s0, 0x48000
	s_mov_b32 s78, 0x50000
	s_mov_b32 s79, 0x58000
	s_mov_b32 s30, 0x60000
	s_mov_b32 s31, 0x68000
	s_mov_b32 s73, 0x70000
	s_mov_b32 s77, 0x78000
	v_mov_b32_e32 v67, 0x3c0881c4
	v_mov_b32_e32 v68, 0xbab64f3b
	s_mov_b32 s86, 0x7f800000
	v_mov_b32_e32 v69, 0xbf1f24be
	v_mov_b32_e32 v70, 0x3e642e9d
	v_not_b32_e32 v71, 31
	v_mov_b32_e32 v72, 0x7fc00000
	v_mov_b32_e32 v73, 0xffc00000
	v_mov_b32_e32 v74, 0x43e00000
	s_mov_b32 s87, 0xc3e00000
	s_movk_i32 s68, 0x4000
	s_mov_b32 s92, 0xc000
	s_mov_b32 s93, 0x14000
	s_mov_b32 s35, 0
	s_branch .LBB0_35

.LBB0_35:
	s_cmpk_gt_i32 s75, 0xfff
	s_mov_b64 s[2:3], -1
	s_cbranch_scc0 .LBB0_269
	s_cmpk_gt_u32 s75, 0x11ff
	s_cbranch_scc0 .LBB0_266
	s_cmpk_gt_u32 s75, 0x15ff
	s_cbranch_scc0 .LBB0_263
	s_cmpk_gt_u32 s75, 0x19ff
	s_cbranch_scc0 .LBB0_260
	s_cmpk_gt_u32 s75, 0x1bff
	s_cbranch_scc0 .LBB0_257
	s_cmpk_gt_u32 s75, 0x1cff
	s_cbranch_scc0 .LBB0_254
	s_cmpk_gt_u32 s75, 0x2cff
	s_cbranch_scc0 .LBB0_123
	s_cmpk_gt_u32 s75, 0x2eff
	s_cbranch_scc0 .LBB0_56
	s_cmpk_lt_u32 s75, 0x2f20
	s_cbranch_scc0 .LBB0_45
	s_add_i32 s34, s95, 0xfff44000
	s_lshl_b64 s[2:3], s[34:35], 8
	v_lshl_add_u64 v[120:121], v[36:37], 0, s[2:3]
	v_add_co_u32_e32 v100, vcc, 0x1000, v120
	global_load_dwordx4 v[40:43], v[120:121], off nt
	global_load_dwordx4 v[76:79], v[120:121], off offset:1024 nt
	global_load_dwordx4 v[80:83], v[120:121], off offset:2048 nt
	global_load_dwordx4 v[84:87], v[120:121], off offset:3072 nt
	v_addc_co_u32_e32 v101, vcc, 0, v121, vcc
	v_add_co_u32_e32 v116, vcc, 0x2000, v120
	global_load_dwordx4 v[88:91], v[100:101], off nt
	global_load_dwordx4 v[92:95], v[100:101], off offset:1024 nt
	global_load_dwordx4 v[96:99], v[100:101], off offset:2048 nt
	s_nop 0
	global_load_dwordx4 v[100:103], v[100:101], off offset:3072 nt
	v_addc_co_u32_e32 v117, vcc, 0, v121, vcc
	v_add_co_u32_e32 v132, vcc, 0x3000, v120
	global_load_dwordx4 v[104:107], v[116:117], off nt
	global_load_dwordx4 v[108:111], v[116:117], off offset:1024 nt
	global_load_dwordx4 v[112:115], v[116:117], off offset:2048 nt
	s_nop 0
	global_load_dwordx4 v[116:119], v[116:117], off offset:3072 nt
	v_addc_co_u32_e32 v133, vcc, 0, v121, vcc
	global_load_dwordx4 v[120:123], v[132:133], off nt
	global_load_dwordx4 v[124:127], v[132:133], off offset:1024 nt
	global_load_dwordx4 v[128:131], v[132:133], off offset:2048 nt
	s_nop 0
	global_load_dwordx4 v[132:135], v[132:133], off offset:3072 nt
	v_add_u32_e32 v1, 0x410, v48
	v_add_u32_e32 v75, 0x418, v48
	v_add_u32_e32 v136, 0x820, v48
	v_add_u32_e32 v137, 0x828, v48
	v_add_u32_e32 v138, 0xc30, v48
	v_add_u32_e32 v139, 0xc38, v48
	v_add_u32_e32 v140, 0x1040, v48
	v_add_u32_e32 v141, 0x1048, v48
	v_add_u32_e32 v142, 0x1450, v48
	v_add_u32_e32 v143, 0x1458, v48
	v_add_u32_e32 v144, 0x1860, v48
	v_add_u32_e32 v145, 0x1868, v48
	v_add_u32_e32 v146, 0x1c70, v48
	v_add_u32_e32 v147, 0x1c78, v48
	v_add_u32_e32 v148, 0x2080, v48
	v_add_u32_e32 v149, 0x2088, v48
	v_add_u32_e32 v150, 0x2490, v48
	v_add_u32_e32 v151, 0x2498, v48
	v_add_u32_e32 v152, 0x28a0, v48
	v_add_u32_e32 v153, 0x28a8, v48
	v_add_u32_e32 v154, 0x2cb0, v48
	v_add_u32_e32 v155, 0x2cb8, v48
	v_add_u32_e32 v156, 0x30c0, v48
	v_add_u32_e32 v157, 0x30c8, v48
	v_add_u32_e32 v158, 0x34d0, v48
	v_add_u32_e32 v159, 0x34d8, v48
	v_add_u32_e32 v160, 0x38e0, v48
	s_movk_i32 s2, 0x7fff
	s_waitcnt vmcnt(15)
	ds_write2_b32 v48, v40, v41 offset1:1
	ds_write2_b32 v48, v42, v43 offset0:2 offset1:3
	s_waitcnt vmcnt(14)
	ds_write2_b32 v1, v76, v77 offset1:1
	ds_write2_b32 v75, v78, v79 offset1:1
	s_waitcnt vmcnt(13)
	ds_write2_b32 v136, v80, v81 offset1:1
	ds_write2_b32 v137, v82, v83 offset1:1
	s_waitcnt vmcnt(12)
	ds_write2_b32 v138, v84, v85 offset1:1
	ds_write2_b32 v139, v86, v87 offset1:1
	s_waitcnt vmcnt(11)
	ds_write2_b32 v140, v88, v89 offset1:1
	ds_write2_b32 v141, v90, v91 offset1:1
	s_waitcnt vmcnt(10)
	ds_write2_b32 v142, v92, v93 offset1:1
	ds_write2_b32 v143, v94, v95 offset1:1
	s_waitcnt vmcnt(9)
	ds_write2_b32 v144, v96, v97 offset1:1
	ds_write2_b32 v145, v98, v99 offset1:1
	s_waitcnt vmcnt(8)
	ds_write2_b32 v146, v100, v101 offset1:1
	ds_write2_b32 v147, v102, v103 offset1:1
	s_waitcnt vmcnt(7)
	ds_write2_b32 v148, v104, v105 offset1:1
	ds_write2_b32 v149, v106, v107 offset1:1
	s_waitcnt vmcnt(6)
	ds_write2_b32 v150, v108, v109 offset1:1
	ds_write2_b32 v151, v110, v111 offset1:1
	s_waitcnt vmcnt(5)
	ds_write2_b32 v152, v112, v113 offset1:1
	ds_write2_b32 v153, v114, v115 offset1:1
	s_waitcnt vmcnt(4)
	ds_write2_b32 v154, v116, v117 offset1:1
	ds_write2_b32 v155, v118, v119 offset1:1
	s_waitcnt vmcnt(3)
	ds_write2_b32 v156, v120, v121 offset1:1
	ds_write2_b32 v157, v122, v123 offset1:1
	s_waitcnt vmcnt(2)
	ds_write2_b32 v158, v124, v125 offset1:1
	ds_write2_b32 v159, v126, v127 offset1:1
	s_waitcnt vmcnt(1)
	ds_write2_b32 v160, v128, v129 offset1:1
	v_add_u32_e32 v1, 0x38e8, v48
	ds_write2_b32 v1, v130, v131 offset1:1
	v_add_u32_e32 v1, 0x3cf0, v48
	s_waitcnt vmcnt(0)
	ds_write2_b32 v1, v132, v133 offset1:1
	v_add_u32_e32 v1, 0x3cf8, v48
	ds_write2_b32 v1, v134, v135 offset1:1
	s_waitcnt lgkmcnt(0)
	ds_read2_b32 v[90:91], v49 offset0:195 offset1:203
	v_add_u32_e32 v75, 0x400, v49
	ds_read2_b32 v[92:93], v75 offset0:4 offset1:12
	ds_read2_b32 v[94:95], v75 offset0:69 offset1:77
	ds_read2_b32 v[96:97], v75 offset0:134 offset1:142
	s_waitcnt lgkmcnt(3)
	v_bfe_u32 v76, v90, 16, 1
	v_add3_u32 v76, v90, v76, s2
	v_and_b32_e32 v76, 0xffff0000, v76
	v_sub_f32_e32 v81, v90, v76
	s_waitcnt lgkmcnt(2)
	v_bfe_u32 v76, v92, 16, 1
	v_add3_u32 v76, v92, v76, s2
	v_and_b32_e32 v76, 0xffff0000, v76
	ds_read2_b32 v[86:87], v49 offset0:65 offset1:73
	ds_read2_b32 v[88:89], v49 offset0:130 offset1:138
	v_sub_f32_e32 v82, v92, v76
	s_waitcnt lgkmcnt(3)
	v_bfe_u32 v76, v94, 16, 1
	ds_read2_b32 v[84:85], v49 offset1:8
	v_add3_u32 v76, v94, v76, s2
	ds_read2_b32 v[98:99], v75 offset0:199 offset1:207
	v_and_b32_e32 v76, 0xffff0000, v76
	v_sub_f32_e32 v83, v94, v76
	s_waitcnt lgkmcnt(4)
	v_bfe_u32 v76, v96, 16, 1
	v_add3_u32 v76, v96, v76, s2
	s_waitcnt lgkmcnt(3)
	v_bfe_u32 v42, v86, 16, 1
	s_waitcnt lgkmcnt(2)
	v_bfe_u32 v43, v88, 16, 1
	v_and_b32_e32 v76, 0xffff0000, v76
	s_waitcnt lgkmcnt(1)
	v_bfe_u32 v1, v84, 16, 1
	v_add3_u32 v42, v86, v42, s2
	v_add3_u32 v43, v88, v43, s2
	v_sub_f32_e32 v100, v96, v76
	s_waitcnt lgkmcnt(0)
	v_bfe_u32 v76, v98, 16, 1
	v_add3_u32 v1, v84, v1, s2
	v_and_b32_e32 v42, 0xffff0000, v42
	v_and_b32_e32 v43, 0xffff0000, v43
	v_add3_u32 v76, v98, v76, s2
	v_and_b32_e32 v40, 7, v254
	v_mul_u32_u24_e32 v40, 0x1f0, v40
	v_lshrrev_b32_e32 v41, 3, v254
	v_lshl_add_u32 v40, v41, 4, v40
	v_mov_b32_e32 v41, s34
	v_lshl_add_u32 v40, v41, 6, v40
	v_mov_b32_e32 v41, 0
	v_lshl_add_u64 v[40:41], v[6:7], 0, v[40:41]
	v_and_b32_e32 v1, 0xffff0000, v1
	v_sub_f32_e32 v42, v86, v42
	v_sub_f32_e32 v43, v88, v43
	v_and_b32_e32 v76, 0xffff0000, v76
	v_sub_f32_e32 v1, v84, v1
	v_sub_f32_e32 v101, v98, v76
	v_cvt_pk_bf16_f32 v76, v84, v86
	v_cvt_pk_bf16_f32 v80, v1, v42
	v_cvt_pk_bf16_f32 v81, v43, v81
	v_lshl_add_u64 v[42:43], v[40:41], 0, v[20:21]
	v_cvt_pk_bf16_f32 v77, v88, v90
	v_cvt_pk_bf16_f32 v78, v92, v94
	v_cvt_pk_bf16_f32 v79, v96, v98
	global_store_dwordx4 v[42:43], v[76:79], off
	v_cvt_pk_bf16_f32 v82, v82, v83
	v_cvt_pk_bf16_f32 v83, v100, v101
	v_bfe_u32 v1, v85, 16, 1
	v_add3_u32 v1, v85, v1, s2
	v_add_co_u32_e32 v76, vcc, s1, v42
	v_and_b32_e32 v1, 0xffff0000, v1
	s_nop 0
	v_addc_co_u32_e32 v77, vcc, 0, v43, vcc
	global_store_dwordx4 v[76:77], v[80:83], off
	v_bfe_u32 v76, v87, 16, 1
	v_add3_u32 v76, v87, v76, s2
	v_and_b32_e32 v76, 0xffff0000, v76
	v_sub_f32_e32 v80, v87, v76
	v_bfe_u32 v76, v89, 16, 1
	v_add3_u32 v76, v89, v76, s2
	v_and_b32_e32 v76, 0xffff0000, v76
	v_sub_f32_e32 v81, v89, v76
	v_bfe_u32 v76, v91, 16, 1
	v_add3_u32 v76, v91, v76, s2
	v_and_b32_e32 v76, 0xffff0000, v76
	v_sub_f32_e32 v82, v91, v76
	v_bfe_u32 v76, v93, 16, 1
	v_add3_u32 v76, v93, v76, s2
	v_and_b32_e32 v76, 0xffff0000, v76
	v_sub_f32_e32 v83, v93, v76
	v_bfe_u32 v76, v95, 16, 1
	v_add3_u32 v76, v95, v76, s2
	v_and_b32_e32 v76, 0xffff0000, v76
	v_sub_f32_e32 v84, v95, v76
	v_bfe_u32 v76, v97, 16, 1
	v_add3_u32 v76, v97, v76, s2
	v_and_b32_e32 v76, 0xffff0000, v76
	v_sub_f32_e32 v86, v97, v76
	v_bfe_u32 v76, v99, 16, 1
	v_add3_u32 v76, v99, v76, s2
	v_and_b32_e32 v76, 0xffff0000, v76
	v_sub_f32_e32 v88, v99, v76
	v_cvt_pk_bf16_f32 v76, v85, v87
	v_cvt_pk_bf16_f32 v81, v81, v82
	v_cvt_pk_bf16_f32 v82, v83, v84
	v_cvt_pk_bf16_f32 v83, v86, v88
	ds_read2_b32 v[86:87], v49 offset0:81 offset1:89
	v_sub_f32_e32 v1, v85, v1
	v_lshl_add_u64 v[84:85], v[40:41], 0, v[22:23]
	v_cvt_pk_bf16_f32 v77, v89, v91
	v_cvt_pk_bf16_f32 v78, v93, v95
	v_cvt_pk_bf16_f32 v79, v97, v99
	global_store_dwordx4 v[84:85], v[76:79], off
	ds_read2_b32 v[88:89], v49 offset0:146 offset1:154
	v_cvt_pk_bf16_f32 v80, v1, v80
	ds_read2_b32 v[90:91], v49 offset0:211 offset1:219
	v_add_co_u32_e32 v76, vcc, 0x40080, v42
	ds_read2_b32 v[92:93], v75 offset0:20 offset1:28
	s_nop 0
	v_addc_co_u32_e32 v77, vcc, 0, v43, vcc
	global_store_dwordx4 v[76:77], v[80:83], off
	s_waitcnt lgkmcnt(3)
	v_bfe_u32 v76, v86, 16, 1
	v_add3_u32 v76, v86, v76, s2
	v_and_b32_e32 v76, 0xffff0000, v76
	v_sub_f32_e32 v80, v86, v76
	s_waitcnt lgkmcnt(2)
	v_bfe_u32 v76, v88, 16, 1
	v_add3_u32 v76, v88, v76, s2
	v_and_b32_e32 v76, 0xffff0000, v76
	v_sub_f32_e32 v81, v88, v76
	s_waitcnt lgkmcnt(1)
	v_bfe_u32 v76, v90, 16, 1
	v_add3_u32 v76, v90, v76, s2
	ds_read2_b32 v[94:95], v75 offset0:85 offset1:93
	v_and_b32_e32 v76, 0xffff0000, v76
	v_sub_f32_e32 v82, v90, v76
	s_waitcnt lgkmcnt(1)
	v_bfe_u32 v76, v92, 16, 1
	v_add3_u32 v76, v92, v76, s2
	ds_read2_b32 v[96:97], v75 offset0:150 offset1:158
	v_and_b32_e32 v76, 0xffff0000, v76
	v_sub_f32_e32 v83, v92, v76
	s_waitcnt lgkmcnt(1)
	v_bfe_u32 v76, v94, 16, 1
	v_add3_u32 v76, v94, v76, s2
	ds_read2_b32 v[98:99], v75 offset0:215 offset1:223
	v_and_b32_e32 v76, 0xffff0000, v76
	v_sub_f32_e32 v100, v94, v76
	s_waitcnt lgkmcnt(1)
	v_bfe_u32 v76, v96, 16, 1
	ds_read2_b32 v[84:85], v49 offset0:16 offset1:24
	v_add3_u32 v76, v96, v76, s2
	v_and_b32_e32 v76, 0xffff0000, v76
	v_sub_f32_e32 v101, v96, v76
	s_waitcnt lgkmcnt(1)
	v_bfe_u32 v76, v98, 16, 1
	v_add3_u32 v76, v98, v76, s2
	v_and_b32_e32 v76, 0xffff0000, v76
	s_waitcnt lgkmcnt(0)
	v_bfe_u32 v1, v84, 16, 1
	v_sub_f32_e32 v102, v98, v76
	v_cvt_pk_bf16_f32 v76, v84, v86
	v_cvt_pk_bf16_f32 v81, v81, v82
	v_cvt_pk_bf16_f32 v82, v83, v100
	v_cvt_pk_bf16_f32 v83, v101, v102
	v_lshl_add_u64 v[100:101], v[40:41], 0, v[24:25]
	v_add3_u32 v1, v84, v1, s2
	v_cvt_pk_bf16_f32 v77, v88, v90
	v_cvt_pk_bf16_f32 v78, v92, v94
	v_cvt_pk_bf16_f32 v79, v96, v98
	global_store_dwordx4 v[100:101], v[76:79], off
	v_and_b32_e32 v1, 0xffff0000, v1
	v_sub_f32_e32 v1, v84, v1
	v_add_co_u32_e32 v76, vcc, 0x40100, v42
	v_cvt_pk_bf16_f32 v80, v1, v80
	v_bfe_u32 v1, v85, 16, 1
	s_nop 0
	v_addc_co_u32_e32 v77, vcc, 0, v43, vcc
	global_store_dwordx4 v[76:77], v[80:83], off
	v_bfe_u32 v76, v87, 16, 1
	v_add3_u32 v76, v87, v76, s2
	v_and_b32_e32 v76, 0xffff0000, v76
	v_sub_f32_e32 v80, v87, v76
	v_bfe_u32 v76, v89, 16, 1
	v_add3_u32 v76, v89, v76, s2
	v_and_b32_e32 v76, 0xffff0000, v76
	v_sub_f32_e32 v81, v89, v76
	v_bfe_u32 v76, v91, 16, 1
	v_add3_u32 v76, v91, v76, s2
	v_and_b32_e32 v76, 0xffff0000, v76
	v_sub_f32_e32 v82, v91, v76
	v_bfe_u32 v76, v93, 16, 1
	v_add3_u32 v76, v93, v76, s2
	v_and_b32_e32 v76, 0xffff0000, v76
	v_sub_f32_e32 v83, v93, v76
	v_bfe_u32 v76, v95, 16, 1
	v_add3_u32 v76, v95, v76, s2
	v_and_b32_e32 v76, 0xffff0000, v76
	v_sub_f32_e32 v84, v95, v76
	v_bfe_u32 v76, v97, 16, 1
	v_add3_u32 v76, v97, v76, s2
	v_and_b32_e32 v76, 0xffff0000, v76
	v_sub_f32_e32 v86, v97, v76
	v_bfe_u32 v76, v99, 16, 1
	v_add3_u32 v76, v99, v76, s2
	v_and_b32_e32 v76, 0xffff0000, v76
	v_add3_u32 v1, v85, v1, s2
	v_sub_f32_e32 v88, v99, v76
	v_cvt_pk_bf16_f32 v76, v85, v87
	v_cvt_pk_bf16_f32 v81, v81, v82
	v_cvt_pk_bf16_f32 v82, v83, v84
	v_cvt_pk_bf16_f32 v83, v86, v88
	ds_read2_b32 v[86:87], v49 offset0:97 offset1:105
	v_and_b32_e32 v1, 0xffff0000, v1
	v_sub_f32_e32 v1, v85, v1
	v_lshl_add_u64 v[84:85], v[40:41], 0, v[26:27]
	v_cvt_pk_bf16_f32 v77, v89, v91
	v_cvt_pk_bf16_f32 v78, v93, v95
	v_cvt_pk_bf16_f32 v79, v97, v99
	global_store_dwordx4 v[84:85], v[76:79], off
	ds_read2_b32 v[88:89], v49 offset0:162 offset1:170
	v_cvt_pk_bf16_f32 v80, v1, v80
	ds_read2_b32 v[90:91], v49 offset0:227 offset1:235
	v_add_co_u32_e32 v76, vcc, 0x40180, v42
	ds_read2_b32 v[92:93], v75 offset0:36 offset1:44
	s_nop 0
	v_addc_co_u32_e32 v77, vcc, 0, v43, vcc
	global_store_dwordx4 v[76:77], v[80:83], off
	s_waitcnt lgkmcnt(3)
	v_bfe_u32 v76, v86, 16, 1
	v_add3_u32 v76, v86, v76, s2
	v_and_b32_e32 v76, 0xffff0000, v76
	v_sub_f32_e32 v80, v86, v76
	s_waitcnt lgkmcnt(2)
	v_bfe_u32 v76, v88, 16, 1
	v_add3_u32 v76, v88, v76, s2
	v_and_b32_e32 v76, 0xffff0000, v76
	v_sub_f32_e32 v81, v88, v76
	s_waitcnt lgkmcnt(1)
	v_bfe_u32 v76, v90, 16, 1
	v_add3_u32 v76, v90, v76, s2
	ds_read2_b32 v[94:95], v75 offset0:101 offset1:109
	v_and_b32_e32 v76, 0xffff0000, v76
	v_sub_f32_e32 v82, v90, v76
	s_waitcnt lgkmcnt(1)
	v_bfe_u32 v76, v92, 16, 1
	v_add3_u32 v76, v92, v76, s2
	ds_read2_b32 v[96:97], v75 offset0:166 offset1:174
	v_and_b32_e32 v76, 0xffff0000, v76
	v_sub_f32_e32 v83, v92, v76
	s_waitcnt lgkmcnt(1)
	v_bfe_u32 v76, v94, 16, 1
	v_add3_u32 v76, v94, v76, s2
	ds_read2_b32 v[98:99], v75 offset0:231 offset1:239
	v_and_b32_e32 v76, 0xffff0000, v76
	v_sub_f32_e32 v100, v94, v76
	s_waitcnt lgkmcnt(1)
	v_bfe_u32 v76, v96, 16, 1
	ds_read2_b32 v[84:85], v49 offset0:32 offset1:40
	v_add3_u32 v76, v96, v76, s2
	v_and_b32_e32 v76, 0xffff0000, v76
	v_sub_f32_e32 v101, v96, v76
	s_waitcnt lgkmcnt(1)
	v_bfe_u32 v76, v98, 16, 1
	v_add3_u32 v76, v98, v76, s2
	v_and_b32_e32 v76, 0xffff0000, v76
	s_waitcnt lgkmcnt(0)
	v_bfe_u32 v1, v84, 16, 1
	v_sub_f32_e32 v102, v98, v76
	v_cvt_pk_bf16_f32 v76, v84, v86
	v_cvt_pk_bf16_f32 v81, v81, v82
	v_cvt_pk_bf16_f32 v82, v83, v100
	v_cvt_pk_bf16_f32 v83, v101, v102
	v_lshl_add_u64 v[100:101], v[40:41], 0, v[28:29]
	v_add3_u32 v1, v84, v1, s2
	v_cvt_pk_bf16_f32 v77, v88, v90
	v_cvt_pk_bf16_f32 v78, v92, v94
	v_cvt_pk_bf16_f32 v79, v96, v98
	global_store_dwordx4 v[100:101], v[76:79], off
	v_and_b32_e32 v1, 0xffff0000, v1
	v_sub_f32_e32 v1, v84, v1
	v_add_co_u32_e32 v76, vcc, 0x60000, v42
	v_cvt_pk_bf16_f32 v80, v1, v80
	v_bfe_u32 v1, v85, 16, 1
	s_nop 0
	v_addc_co_u32_e32 v77, vcc, 0, v43, vcc
	global_store_dwordx4 v[76:77], v[80:83], off
	v_bfe_u32 v76, v87, 16, 1
	v_add3_u32 v76, v87, v76, s2
	v_and_b32_e32 v76, 0xffff0000, v76
	v_sub_f32_e32 v80, v87, v76
	v_bfe_u32 v76, v89, 16, 1
	v_add3_u32 v76, v89, v76, s2
	v_and_b32_e32 v76, 0xffff0000, v76
	v_sub_f32_e32 v81, v89, v76
	v_bfe_u32 v76, v91, 16, 1
	v_add3_u32 v76, v91, v76, s2
	v_and_b32_e32 v76, 0xffff0000, v76
	v_sub_f32_e32 v82, v91, v76
	v_bfe_u32 v76, v93, 16, 1
	v_add3_u32 v76, v93, v76, s2
	v_and_b32_e32 v76, 0xffff0000, v76
	v_sub_f32_e32 v83, v93, v76
	v_bfe_u32 v76, v95, 16, 1
	v_add3_u32 v76, v95, v76, s2
	v_and_b32_e32 v76, 0xffff0000, v76
	v_sub_f32_e32 v84, v95, v76
	v_bfe_u32 v76, v97, 16, 1
	v_add3_u32 v76, v97, v76, s2
	v_and_b32_e32 v76, 0xffff0000, v76
	v_sub_f32_e32 v86, v97, v76
	v_bfe_u32 v76, v99, 16, 1
	v_add3_u32 v76, v99, v76, s2
	v_and_b32_e32 v76, 0xffff0000, v76
	v_add3_u32 v1, v85, v1, s2
	v_sub_f32_e32 v88, v99, v76
	v_cvt_pk_bf16_f32 v76, v85, v87
	v_cvt_pk_bf16_f32 v81, v81, v82
	v_cvt_pk_bf16_f32 v82, v83, v84
	v_cvt_pk_bf16_f32 v83, v86, v88
	ds_read2_b32 v[86:87], v49 offset0:113 offset1:121
	v_and_b32_e32 v1, 0xffff0000, v1
	v_sub_f32_e32 v1, v85, v1
	v_lshl_add_u64 v[84:85], v[40:41], 0, v[30:31]
	v_cvt_pk_bf16_f32 v77, v89, v91
	v_cvt_pk_bf16_f32 v78, v93, v95
	v_cvt_pk_bf16_f32 v79, v97, v99
	global_store_dwordx4 v[84:85], v[76:79], off
	ds_read2_b32 v[88:89], v49 offset0:178 offset1:186
	v_cvt_pk_bf16_f32 v80, v1, v80
	ds_read2_b32 v[90:91], v49 offset0:243 offset1:251
	v_add_co_u32_e32 v76, vcc, 0x60080, v42
	ds_read2_b32 v[92:93], v75 offset0:52 offset1:60
	s_nop 0
	v_addc_co_u32_e32 v77, vcc, 0, v43, vcc
	global_store_dwordx4 v[76:77], v[80:83], off
	s_waitcnt lgkmcnt(3)
	v_bfe_u32 v76, v86, 16, 1
	v_add3_u32 v76, v86, v76, s2
	v_and_b32_e32 v76, 0xffff0000, v76
	v_sub_f32_e32 v80, v86, v76
	s_waitcnt lgkmcnt(2)
	v_bfe_u32 v76, v88, 16, 1
	v_add3_u32 v76, v88, v76, s2
	v_and_b32_e32 v76, 0xffff0000, v76
	v_sub_f32_e32 v81, v88, v76
	s_waitcnt lgkmcnt(1)
	v_bfe_u32 v76, v90, 16, 1
	v_add3_u32 v76, v90, v76, s2
	ds_read2_b32 v[94:95], v75 offset0:117 offset1:125
	v_and_b32_e32 v76, 0xffff0000, v76
	v_sub_f32_e32 v82, v90, v76
	s_waitcnt lgkmcnt(1)
	v_bfe_u32 v76, v92, 16, 1
	v_add3_u32 v76, v92, v76, s2
	ds_read2_b32 v[98:99], v75 offset0:247 offset1:255
	v_and_b32_e32 v76, 0xffff0000, v76
	ds_read2_b32 v[96:97], v75 offset0:182 offset1:190
	v_sub_f32_e32 v83, v92, v76
	s_waitcnt lgkmcnt(2)
	v_bfe_u32 v76, v94, 16, 1
	v_add3_u32 v76, v94, v76, s2
	ds_read2_b32 v[84:85], v49 offset0:48 offset1:56
	v_and_b32_e32 v76, 0xffff0000, v76
	v_sub_f32_e32 v100, v94, v76
	s_waitcnt lgkmcnt(2)
	v_bfe_u32 v76, v98, 16, 1
	s_waitcnt lgkmcnt(1)
	v_bfe_u32 v75, v96, 16, 1
	v_add3_u32 v76, v98, v76, s2
	v_add3_u32 v75, v96, v75, s2
	v_and_b32_e32 v76, 0xffff0000, v76
	v_and_b32_e32 v75, 0xffff0000, v75
	v_sub_f32_e32 v101, v98, v76
	s_waitcnt lgkmcnt(0)
	v_bfe_u32 v1, v84, 16, 1
	v_sub_f32_e32 v75, v96, v75
	v_cvt_pk_bf16_f32 v76, v84, v86
	v_cvt_pk_bf16_f32 v81, v81, v82
	v_cvt_pk_bf16_f32 v82, v83, v100
	v_cvt_pk_bf16_f32 v83, v75, v101
	v_lshl_add_u64 v[100:101], v[40:41], 0, v[32:33]
	v_add3_u32 v1, v84, v1, s2
	v_cvt_pk_bf16_f32 v77, v88, v90
	v_cvt_pk_bf16_f32 v78, v92, v94
	v_cvt_pk_bf16_f32 v79, v96, v98
	global_store_dwordx4 v[100:101], v[76:79], off
	v_and_b32_e32 v1, 0xffff0000, v1
	v_sub_f32_e32 v1, v84, v1
	v_add_co_u32_e32 v76, vcc, 0x60100, v42
	v_cvt_pk_bf16_f32 v80, v1, v80
	v_bfe_u32 v1, v85, 16, 1
	s_nop 0
	v_addc_co_u32_e32 v77, vcc, 0, v43, vcc
	global_store_dwordx4 v[76:77], v[80:83], off
	v_bfe_u32 v76, v89, 16, 1
	v_add3_u32 v76, v89, v76, s2
	v_and_b32_e32 v76, 0xffff0000, v76
	v_sub_f32_e32 v81, v89, v76
	v_bfe_u32 v76, v91, 16, 1
	v_add3_u32 v76, v91, v76, s2
	v_and_b32_e32 v76, 0xffff0000, v76
	v_sub_f32_e32 v82, v91, v76
	v_bfe_u32 v76, v93, 16, 1
	v_add3_u32 v76, v93, v76, s2
	v_and_b32_e32 v76, 0xffff0000, v76
	v_sub_f32_e32 v83, v93, v76
	v_bfe_u32 v76, v95, 16, 1
	v_add3_u32 v76, v95, v76, s2
	v_and_b32_e32 v76, 0xffff0000, v76
	v_sub_f32_e32 v84, v95, v76
	v_bfe_u32 v76, v97, 16, 1
	v_add3_u32 v76, v97, v76, s2
	v_and_b32_e32 v76, 0xffff0000, v76
	v_sub_f32_e32 v86, v97, v76
	v_bfe_u32 v76, v99, 16, 1
	v_add3_u32 v76, v99, v76, s2
	v_bfe_u32 v75, v87, 16, 1
	v_and_b32_e32 v76, 0xffff0000, v76
	v_lshl_add_u64 v[40:41], v[40:41], 0, v[34:35]
	v_add3_u32 v1, v85, v1, s2
	v_add3_u32 v75, v87, v75, s2
	v_sub_f32_e32 v88, v99, v76
	v_cvt_pk_bf16_f32 v76, v85, v87
	v_cvt_pk_bf16_f32 v77, v89, v91
	v_cvt_pk_bf16_f32 v78, v93, v95
	v_cvt_pk_bf16_f32 v79, v97, v99
	global_store_dwordx4 v[40:41], v[76:79], off
	v_add_co_u32_e32 v40, vcc, 0x60180, v42
	v_and_b32_e32 v1, 0xffff0000, v1
	v_and_b32_e32 v75, 0xffff0000, v75
	v_addc_co_u32_e32 v41, vcc, 0, v43, vcc
	v_sub_f32_e32 v1, v85, v1
	v_sub_f32_e32 v75, v87, v75
	v_cvt_pk_bf16_f32 v80, v1, v75
	v_cvt_pk_bf16_f32 v81, v81, v82
	v_cvt_pk_bf16_f32 v82, v83, v84
	v_cvt_pk_bf16_f32 v83, v86, v88
	global_store_dwordx4 v[40:41], v[80:83], off
	s_waitcnt lgkmcnt(0)
	s_mov_b64 s[2:3], 0

.LBB0_1875:
	s_lshl_b32 s87, s86, 5
	s_add_i32 s60, s87, s65
	s_ashr_i32 s61, s60, 31
	s_lshl_b64 s[34:35], s[60:61], 12
	v_lshl_add_u64 v[14:15], v[44:45], 0, s[34:35]
	v_lshl_add_u64 v[160:161], v[44:45], 0, s[34:35]
	global_load_dwordx4 v[2:5], v[14:15], off
	global_load_dwordx4 v[6:9], v[14:15], off offset:1024
	global_load_dwordx4 v[10:13], v[14:15], off offset:2048
	s_nop 0
	global_load_dwordx4 v[14:17], v[14:15], off offset:3072
	v_add_co_u32_e32 v162, vcc, 0x1000, v160
	s_nop 1
	v_addc_co_u32_e32 v163, vcc, 0, v161, vcc
	global_load_dwordx4 v[112:115], v[162:163], off
	global_load_dwordx4 v[116:119], v[162:163], off offset:1024
	global_load_dwordx4 v[120:123], v[162:163], off offset:2048
	global_load_dwordx4 v[124:127], v[162:163], off offset:3072
	v_add_co_u32_e32 v164, vcc, 0x2000, v160
	s_nop 1
	v_addc_co_u32_e32 v165, vcc, 0, v161, vcc
	global_load_dwordx4 v[128:131], v[164:165], off
	global_load_dwordx4 v[132:135], v[164:165], off offset:1024
	global_load_dwordx4 v[136:139], v[164:165], off offset:2048
	global_load_dwordx4 v[140:143], v[164:165], off offset:3072
	v_add_co_u32_e32 v166, vcc, 0x3000, v160
	s_nop 1
	v_addc_co_u32_e32 v167, vcc, 0, v161, vcc
	global_load_dwordx4 v[144:147], v[166:167], off
	global_load_dwordx4 v[148:151], v[166:167], off offset:1024
	global_load_dwordx4 v[152:155], v[166:167], off offset:2048
	global_load_dwordx4 v[156:159], v[166:167], off offset:3072
	s_waitcnt vmcnt(15)
	v_lshlrev_b32_e32 v1, 16, v2
	v_and_b32_e32 v2, 0xffff0000, v2
	v_mul_f32_e32 v2, v2, v2
	v_lshlrev_b32_e32 v18, 16, v3
	v_fmac_f32_e32 v2, v1, v1
	v_and_b32_e32 v3, 0xffff0000, v3
	v_fmac_f32_e32 v2, v18, v18
	v_lshlrev_b32_e32 v19, 16, v4
	v_fmac_f32_e32 v2, v3, v3
	v_and_b32_e32 v4, 0xffff0000, v4
	v_fmac_f32_e32 v2, v19, v19
	v_lshlrev_b32_e32 v20, 16, v5
	v_fmac_f32_e32 v2, v4, v4
	v_and_b32_e32 v5, 0xffff0000, v5
	v_fmac_f32_e32 v2, v20, v20
	s_waitcnt vmcnt(14)
	v_lshlrev_b32_e32 v21, 16, v6
	v_fmac_f32_e32 v2, v5, v5
	v_and_b32_e32 v6, 0xffff0000, v6
	v_fmac_f32_e32 v2, v21, v21
	v_lshlrev_b32_e32 v22, 16, v7
	v_fmac_f32_e32 v2, v6, v6
	v_and_b32_e32 v7, 0xffff0000, v7
	v_fmac_f32_e32 v2, v22, v22
	v_lshlrev_b32_e32 v23, 16, v8
	v_fmac_f32_e32 v2, v7, v7
	v_and_b32_e32 v8, 0xffff0000, v8
	v_fmac_f32_e32 v2, v23, v23
	v_lshlrev_b32_e32 v24, 16, v9
	v_fmac_f32_e32 v2, v8, v8
	v_and_b32_e32 v9, 0xffff0000, v9
	v_fmac_f32_e32 v2, v24, v24
	s_waitcnt vmcnt(13)
	v_lshlrev_b32_e32 v25, 16, v10
	v_fmac_f32_e32 v2, v9, v9
	v_and_b32_e32 v10, 0xffff0000, v10
	v_fmac_f32_e32 v2, v25, v25
	v_lshlrev_b32_e32 v26, 16, v11
	v_fmac_f32_e32 v2, v10, v10
	v_and_b32_e32 v11, 0xffff0000, v11
	v_fmac_f32_e32 v2, v26, v26
	v_lshlrev_b32_e32 v27, 16, v12
	v_fmac_f32_e32 v2, v11, v11
	v_and_b32_e32 v12, 0xffff0000, v12
	v_fmac_f32_e32 v2, v27, v27
	v_lshlrev_b32_e32 v28, 16, v13
	v_fmac_f32_e32 v2, v12, v12
	v_and_b32_e32 v13, 0xffff0000, v13
	v_fmac_f32_e32 v2, v28, v28
	s_waitcnt vmcnt(12)
	v_lshlrev_b32_e32 v29, 16, v14
	v_fmac_f32_e32 v2, v13, v13
	v_and_b32_e32 v14, 0xffff0000, v14
	v_fmac_f32_e32 v2, v29, v29
	v_lshlrev_b32_e32 v30, 16, v15
	v_fmac_f32_e32 v2, v14, v14
	v_and_b32_e32 v15, 0xffff0000, v15
	v_fmac_f32_e32 v2, v30, v30
	v_lshlrev_b32_e32 v31, 16, v16
	v_fmac_f32_e32 v2, v15, v15
	v_and_b32_e32 v16, 0xffff0000, v16
	v_fmac_f32_e32 v2, v31, v31
	v_lshlrev_b32_e32 v32, 16, v17
	v_fmac_f32_e32 v2, v16, v16
	v_and_b32_e32 v1, 0xffff0000, v17
	v_fmac_f32_e32 v2, v32, v32
	v_fmac_f32_e32 v2, v1, v1
	ds_bpermute_b32 v1, v76, v2
	s_waitcnt lgkmcnt(0)
	v_add_f32_e32 v1, v2, v1
	ds_bpermute_b32 v2, v77, v1
	s_waitcnt lgkmcnt(0)
	v_add_f32_e32 v1, v1, v2
	ds_bpermute_b32 v2, v78, v1
	s_waitcnt lgkmcnt(0)
	v_add_f32_e32 v1, v1, v2
	ds_bpermute_b32 v2, v79, v1
	s_waitcnt lgkmcnt(0)
	v_add_f32_e32 v1, v1, v2
	ds_bpermute_b32 v2, v80, v1
	s_waitcnt lgkmcnt(0)
	v_add_f32_e32 v2, v1, v2
	ds_bpermute_b32 v3, v81, v2
	s_and_saveexec_b64 s[36:37], s[2:3]
	s_cbranch_execz .LBB0_1877
	s_waitcnt lgkmcnt(0)
	v_add_f32_e32 v1, v2, v3
	v_fmamk_f32 v1, v1, 0x3a000000, v105
	v_mul_f32_e32 v2, 0x4f800000, v1
	v_cmp_gt_f32_e32 vcc, s81, v1
	s_nop 1
	v_cndmask_b32_e32 v1, v1, v2, vcc
	v_sqrt_f32_e32 v2, v1
	s_nop 0
	v_add_u32_e32 v3, -1, v2
	v_fma_f32 v5, -v3, v2, v1
	v_add_u32_e32 v4, 1, v2
	v_cmp_ge_f32_e64 s[34:35], 0, v5
	s_nop 1
	v_cndmask_b32_e64 v3, v2, v3, s[34:35]
	v_fma_f32 v2, -v4, v2, v1
	v_cmp_lt_f32_e64 s[34:35], 0, v2
	s_nop 1
	v_cndmask_b32_e64 v2, v3, v4, s[34:35]
	v_mul_f32_e32 v3, 0x37800000, v2
	v_cndmask_b32_e32 v2, v2, v3, vcc
	v_cmp_class_f32_e32 vcc, v1, v106
	s_nop 1
	v_cndmask_b32_e32 v1, v2, v1, vcc
	v_div_scale_f32 v2, s[34:35], v1, v1, 1.0
	v_rcp_f32_e32 v3, v2
	s_nop 0
	v_fma_f32 v4, -v2, v3, 1.0
	v_fmac_f32_e32 v3, v4, v3
	v_div_scale_f32 v4, vcc, 1.0, v1, 1.0
	v_mul_f32_e32 v5, v4, v3
	v_fma_f32 v6, -v2, v5, v4
	v_fmac_f32_e32 v5, v6, v3
	v_fma_f32 v2, -v2, v5, v4
	v_div_fmas_f32 v2, v2, v3, v5
	v_div_fixup_f32 v1, v2, v1, 1.0
	v_mov_b32_e32 v2, s68
	ds_write_b32 v2, v1
.LBB0_1877:
	s_or_b64 exec, exec, s[36:37]
	s_or_b32 s34, s60, 1
	s_ashr_i32 s35, s34, 31
	s_lshl_b64 s[34:35], s[34:35], 12
	s_waitcnt lgkmcnt(0)
	s_waitcnt vmcnt(8)
	v_mov_b32_e32 v2, v112
	v_mov_b32_e32 v3, v113
	v_mov_b32_e32 v4, v114
	v_mov_b32_e32 v5, v115
	v_mov_b32_e32 v6, v116
	v_mov_b32_e32 v7, v117
	v_mov_b32_e32 v8, v118
	v_mov_b32_e32 v9, v119
	v_mov_b32_e32 v10, v120
	v_mov_b32_e32 v11, v121
	v_mov_b32_e32 v12, v122
	v_mov_b32_e32 v13, v123
	v_mov_b32_e32 v14, v124
	v_mov_b32_e32 v15, v125
	v_mov_b32_e32 v16, v126
	v_mov_b32_e32 v17, v127
	s_nop 0
	v_lshlrev_b32_e32 v1, 16, v2
	v_and_b32_e32 v2, 0xffff0000, v2
	v_mul_f32_e32 v2, v2, v2
	v_lshlrev_b32_e32 v18, 16, v3
	v_fmac_f32_e32 v2, v1, v1
	v_and_b32_e32 v3, 0xffff0000, v3
	v_fmac_f32_e32 v2, v18, v18
	v_lshlrev_b32_e32 v19, 16, v4
	v_fmac_f32_e32 v2, v3, v3
	v_and_b32_e32 v4, 0xffff0000, v4
	v_fmac_f32_e32 v2, v19, v19
	v_lshlrev_b32_e32 v20, 16, v5
	v_fmac_f32_e32 v2, v4, v4
	v_and_b32_e32 v5, 0xffff0000, v5
	v_fmac_f32_e32 v2, v20, v20
	v_lshlrev_b32_e32 v21, 16, v6
	v_fmac_f32_e32 v2, v5, v5
	v_and_b32_e32 v6, 0xffff0000, v6
	v_fmac_f32_e32 v2, v21, v21
	v_lshlrev_b32_e32 v22, 16, v7
	v_fmac_f32_e32 v2, v6, v6
	v_and_b32_e32 v7, 0xffff0000, v7
	v_fmac_f32_e32 v2, v22, v22
	v_lshlrev_b32_e32 v23, 16, v8
	v_fmac_f32_e32 v2, v7, v7
	v_and_b32_e32 v8, 0xffff0000, v8
	v_fmac_f32_e32 v2, v23, v23
	v_lshlrev_b32_e32 v24, 16, v9
	v_fmac_f32_e32 v2, v8, v8
	v_and_b32_e32 v9, 0xffff0000, v9
	v_fmac_f32_e32 v2, v24, v24
	v_lshlrev_b32_e32 v25, 16, v10
	v_fmac_f32_e32 v2, v9, v9
	v_and_b32_e32 v10, 0xffff0000, v10
	v_fmac_f32_e32 v2, v25, v25
	v_lshlrev_b32_e32 v26, 16, v11
	v_fmac_f32_e32 v2, v10, v10
	v_and_b32_e32 v11, 0xffff0000, v11
	v_fmac_f32_e32 v2, v26, v26
	v_lshlrev_b32_e32 v27, 16, v12
	v_fmac_f32_e32 v2, v11, v11
	v_and_b32_e32 v12, 0xffff0000, v12
	v_fmac_f32_e32 v2, v27, v27
	v_lshlrev_b32_e32 v28, 16, v13
	v_fmac_f32_e32 v2, v12, v12
	v_and_b32_e32 v13, 0xffff0000, v13
	v_fmac_f32_e32 v2, v28, v28
	v_lshlrev_b32_e32 v29, 16, v14
	v_fmac_f32_e32 v2, v13, v13
	v_and_b32_e32 v14, 0xffff0000, v14
	v_fmac_f32_e32 v2, v29, v29
	v_lshlrev_b32_e32 v30, 16, v15
	v_fmac_f32_e32 v2, v14, v14
	v_and_b32_e32 v15, 0xffff0000, v15
	v_fmac_f32_e32 v2, v30, v30
	v_lshlrev_b32_e32 v31, 16, v16
	v_fmac_f32_e32 v2, v15, v15
	v_and_b32_e32 v16, 0xffff0000, v16
	v_fmac_f32_e32 v2, v31, v31
	v_lshlrev_b32_e32 v32, 16, v17
	v_fmac_f32_e32 v2, v16, v16
	v_and_b32_e32 v1, 0xffff0000, v17
	v_fmac_f32_e32 v2, v32, v32
	v_fmac_f32_e32 v2, v1, v1
	ds_bpermute_b32 v1, v76, v2
	s_waitcnt lgkmcnt(0)
	v_add_f32_e32 v1, v2, v1
	ds_bpermute_b32 v2, v77, v1
	s_waitcnt lgkmcnt(0)
	v_add_f32_e32 v1, v1, v2
	ds_bpermute_b32 v2, v78, v1
	s_waitcnt lgkmcnt(0)
	v_add_f32_e32 v1, v1, v2
	ds_bpermute_b32 v2, v79, v1
	s_waitcnt lgkmcnt(0)
	v_add_f32_e32 v1, v1, v2
	ds_bpermute_b32 v2, v80, v1
	s_waitcnt lgkmcnt(0)
	v_add_f32_e32 v2, v1, v2
	ds_bpermute_b32 v3, v81, v2
	s_and_saveexec_b64 s[36:37], s[2:3]
	s_cbranch_execz .LBB0_1879
	s_waitcnt lgkmcnt(0)
	v_add_f32_e32 v1, v2, v3
	v_fmamk_f32 v1, v1, 0x3a000000, v105
	v_mul_f32_e32 v2, 0x4f800000, v1
	v_cmp_gt_f32_e32 vcc, s81, v1
	s_nop 1
	v_cndmask_b32_e32 v1, v1, v2, vcc
	v_sqrt_f32_e32 v2, v1
	s_nop 0
	v_add_u32_e32 v3, -1, v2
	v_fma_f32 v5, -v3, v2, v1
	v_add_u32_e32 v4, 1, v2
	v_cmp_ge_f32_e64 s[34:35], 0, v5
	s_nop 1
	v_cndmask_b32_e64 v3, v2, v3, s[34:35]
	v_fma_f32 v2, -v4, v2, v1
	v_cmp_lt_f32_e64 s[34:35], 0, v2
	s_nop 1
	v_cndmask_b32_e64 v2, v3, v4, s[34:35]
	v_mul_f32_e32 v3, 0x37800000, v2
	v_cndmask_b32_e32 v2, v2, v3, vcc
	v_cmp_class_f32_e32 vcc, v1, v106
	s_nop 1
	v_cndmask_b32_e32 v1, v2, v1, vcc
	v_div_scale_f32 v2, s[34:35], v1, v1, 1.0
	v_rcp_f32_e32 v3, v2
	s_nop 0
	v_fma_f32 v4, -v2, v3, 1.0
	v_fmac_f32_e32 v3, v4, v3
	v_div_scale_f32 v4, vcc, 1.0, v1, 1.0
	v_mul_f32_e32 v5, v4, v3
	v_fma_f32 v6, -v2, v5, v4
	v_fmac_f32_e32 v5, v6, v3
	v_fma_f32 v2, -v2, v5, v4
	v_div_fmas_f32 v2, v2, v3, v5
	v_div_fixup_f32 v1, v2, v1, 1.0
	v_mov_b32_e32 v2, s68
	ds_write_b32 v2, v1 offset:4
.LBB0_1879:
	s_or_b64 exec, exec, s[36:37]
	s_or_b32 s34, s60, 2
	s_ashr_i32 s35, s34, 31
	s_lshl_b64 s[34:35], s[34:35], 12
	s_waitcnt lgkmcnt(0)
	s_waitcnt vmcnt(4)
	v_mov_b32_e32 v2, v128
	v_mov_b32_e32 v3, v129
	v_mov_b32_e32 v4, v130
	v_mov_b32_e32 v5, v131
	v_mov_b32_e32 v6, v132
	v_mov_b32_e32 v7, v133
	v_mov_b32_e32 v8, v134
	v_mov_b32_e32 v9, v135
	v_mov_b32_e32 v10, v136
	v_mov_b32_e32 v11, v137
	v_mov_b32_e32 v12, v138
	v_mov_b32_e32 v13, v139
	v_mov_b32_e32 v14, v140
	v_mov_b32_e32 v15, v141
	v_mov_b32_e32 v16, v142
	v_mov_b32_e32 v17, v143
	s_nop 0
	v_lshlrev_b32_e32 v1, 16, v2
	v_and_b32_e32 v2, 0xffff0000, v2
	v_mul_f32_e32 v2, v2, v2
	v_lshlrev_b32_e32 v18, 16, v3
	v_fmac_f32_e32 v2, v1, v1
	v_and_b32_e32 v3, 0xffff0000, v3
	v_fmac_f32_e32 v2, v18, v18
	v_lshlrev_b32_e32 v19, 16, v4
	v_fmac_f32_e32 v2, v3, v3
	v_and_b32_e32 v4, 0xffff0000, v4
	v_fmac_f32_e32 v2, v19, v19
	v_lshlrev_b32_e32 v20, 16, v5
	v_fmac_f32_e32 v2, v4, v4
	v_and_b32_e32 v5, 0xffff0000, v5
	v_fmac_f32_e32 v2, v20, v20
	v_lshlrev_b32_e32 v21, 16, v6
	v_fmac_f32_e32 v2, v5, v5
	v_and_b32_e32 v6, 0xffff0000, v6
	v_fmac_f32_e32 v2, v21, v21
	v_lshlrev_b32_e32 v22, 16, v7
	v_fmac_f32_e32 v2, v6, v6
	v_and_b32_e32 v7, 0xffff0000, v7
	v_fmac_f32_e32 v2, v22, v22
	v_lshlrev_b32_e32 v23, 16, v8
	v_fmac_f32_e32 v2, v7, v7
	v_and_b32_e32 v8, 0xffff0000, v8
	v_fmac_f32_e32 v2, v23, v23
	v_lshlrev_b32_e32 v24, 16, v9
	v_fmac_f32_e32 v2, v8, v8
	v_and_b32_e32 v9, 0xffff0000, v9
	v_fmac_f32_e32 v2, v24, v24
	v_lshlrev_b32_e32 v25, 16, v10
	v_fmac_f32_e32 v2, v9, v9
	v_and_b32_e32 v10, 0xffff0000, v10
	v_fmac_f32_e32 v2, v25, v25
	v_lshlrev_b32_e32 v26, 16, v11
	v_fmac_f32_e32 v2, v10, v10
	v_and_b32_e32 v11, 0xffff0000, v11
	v_fmac_f32_e32 v2, v26, v26
	v_lshlrev_b32_e32 v27, 16, v12
	v_fmac_f32_e32 v2, v11, v11
	v_and_b32_e32 v12, 0xffff0000, v12
	v_fmac_f32_e32 v2, v27, v27
	v_lshlrev_b32_e32 v28, 16, v13
	v_fmac_f32_e32 v2, v12, v12
	v_and_b32_e32 v13, 0xffff0000, v13
	v_fmac_f32_e32 v2, v28, v28
	v_lshlrev_b32_e32 v29, 16, v14
	v_fmac_f32_e32 v2, v13, v13
	v_and_b32_e32 v14, 0xffff0000, v14
	v_fmac_f32_e32 v2, v29, v29
	v_lshlrev_b32_e32 v30, 16, v15
	v_fmac_f32_e32 v2, v14, v14
	v_and_b32_e32 v15, 0xffff0000, v15
	v_fmac_f32_e32 v2, v30, v30
	v_lshlrev_b32_e32 v31, 16, v16
	v_fmac_f32_e32 v2, v15, v15
	v_and_b32_e32 v16, 0xffff0000, v16
	v_fmac_f32_e32 v2, v31, v31
	v_lshlrev_b32_e32 v32, 16, v17
	v_fmac_f32_e32 v2, v16, v16
	v_and_b32_e32 v1, 0xffff0000, v17
	v_fmac_f32_e32 v2, v32, v32
	v_fmac_f32_e32 v2, v1, v1
	ds_bpermute_b32 v1, v76, v2
	s_waitcnt lgkmcnt(0)
	v_add_f32_e32 v1, v2, v1
	ds_bpermute_b32 v2, v77, v1
	s_waitcnt lgkmcnt(0)
	v_add_f32_e32 v1, v1, v2
	ds_bpermute_b32 v2, v78, v1
	s_waitcnt lgkmcnt(0)
	v_add_f32_e32 v1, v1, v2
	ds_bpermute_b32 v2, v79, v1
	s_waitcnt lgkmcnt(0)
	v_add_f32_e32 v1, v1, v2
	ds_bpermute_b32 v2, v80, v1
	s_waitcnt lgkmcnt(0)
	v_add_f32_e32 v2, v1, v2
	ds_bpermute_b32 v3, v81, v2
	s_and_saveexec_b64 s[36:37], s[2:3]
	s_cbranch_execz .LBB0_1881
	s_waitcnt lgkmcnt(0)
	v_add_f32_e32 v1, v2, v3
	v_fmamk_f32 v1, v1, 0x3a000000, v105
	v_mul_f32_e32 v2, 0x4f800000, v1
	v_cmp_gt_f32_e32 vcc, s81, v1
	s_nop 1
	v_cndmask_b32_e32 v1, v1, v2, vcc
	v_sqrt_f32_e32 v2, v1
	s_nop 0
	v_add_u32_e32 v3, -1, v2
	v_fma_f32 v5, -v3, v2, v1
	v_add_u32_e32 v4, 1, v2
	v_cmp_ge_f32_e64 s[34:35], 0, v5
	s_nop 1
	v_cndmask_b32_e64 v3, v2, v3, s[34:35]
	v_fma_f32 v2, -v4, v2, v1
	v_cmp_lt_f32_e64 s[34:35], 0, v2
	s_nop 1
	v_cndmask_b32_e64 v2, v3, v4, s[34:35]
	v_mul_f32_e32 v3, 0x37800000, v2
	v_cndmask_b32_e32 v2, v2, v3, vcc
	v_cmp_class_f32_e32 vcc, v1, v106
	s_nop 1
	v_cndmask_b32_e32 v1, v2, v1, vcc
	v_div_scale_f32 v2, s[34:35], v1, v1, 1.0
	v_rcp_f32_e32 v3, v2
	s_nop 0
	v_fma_f32 v4, -v2, v3, 1.0
	v_fmac_f32_e32 v3, v4, v3
	v_div_scale_f32 v4, vcc, 1.0, v1, 1.0
	v_mul_f32_e32 v5, v4, v3
	v_fma_f32 v6, -v2, v5, v4
	v_fmac_f32_e32 v5, v6, v3
	v_fma_f32 v2, -v2, v5, v4
	v_div_fmas_f32 v2, v2, v3, v5
	v_div_fixup_f32 v1, v2, v1, 1.0
	v_mov_b32_e32 v2, s68
	ds_write_b32 v2, v1 offset:8
.LBB0_1881:
	s_or_b64 exec, exec, s[36:37]
	s_or_b32 s34, s60, 3
	s_ashr_i32 s35, s34, 31
	s_lshl_b64 s[34:35], s[34:35], 12
	s_waitcnt lgkmcnt(0)
	s_waitcnt vmcnt(0)
	v_mov_b32_e32 v2, v144
	v_mov_b32_e32 v3, v145
	v_mov_b32_e32 v4, v146
	v_mov_b32_e32 v5, v147
	v_mov_b32_e32 v6, v148
	v_mov_b32_e32 v7, v149
	v_mov_b32_e32 v8, v150
	v_mov_b32_e32 v9, v151
	v_mov_b32_e32 v10, v152
	v_mov_b32_e32 v11, v153
	v_mov_b32_e32 v12, v154
	v_mov_b32_e32 v13, v155
	v_mov_b32_e32 v14, v156
	v_mov_b32_e32 v15, v157
	v_mov_b32_e32 v16, v158
	v_mov_b32_e32 v17, v159
	s_nop 0
	v_lshlrev_b32_e32 v1, 16, v2
	v_and_b32_e32 v2, 0xffff0000, v2
	v_mul_f32_e32 v2, v2, v2
	v_lshlrev_b32_e32 v18, 16, v3
	v_fmac_f32_e32 v2, v1, v1
	v_and_b32_e32 v3, 0xffff0000, v3
	v_fmac_f32_e32 v2, v18, v18
	v_lshlrev_b32_e32 v19, 16, v4
	v_fmac_f32_e32 v2, v3, v3
	v_and_b32_e32 v4, 0xffff0000, v4
	v_fmac_f32_e32 v2, v19, v19
	v_lshlrev_b32_e32 v20, 16, v5
	v_fmac_f32_e32 v2, v4, v4
	v_and_b32_e32 v5, 0xffff0000, v5
	v_fmac_f32_e32 v2, v20, v20
	v_lshlrev_b32_e32 v21, 16, v6
	v_fmac_f32_e32 v2, v5, v5
	v_and_b32_e32 v6, 0xffff0000, v6
	v_fmac_f32_e32 v2, v21, v21
	v_lshlrev_b32_e32 v22, 16, v7
	v_fmac_f32_e32 v2, v6, v6
	v_and_b32_e32 v7, 0xffff0000, v7
	v_fmac_f32_e32 v2, v22, v22
	v_lshlrev_b32_e32 v23, 16, v8
	v_fmac_f32_e32 v2, v7, v7
	v_and_b32_e32 v8, 0xffff0000, v8
	v_fmac_f32_e32 v2, v23, v23
	v_lshlrev_b32_e32 v24, 16, v9
	v_fmac_f32_e32 v2, v8, v8
	v_and_b32_e32 v9, 0xffff0000, v9
	v_fmac_f32_e32 v2, v24, v24
	v_lshlrev_b32_e32 v25, 16, v10
	v_fmac_f32_e32 v2, v9, v9
	v_and_b32_e32 v10, 0xffff0000, v10
	v_fmac_f32_e32 v2, v25, v25
	v_lshlrev_b32_e32 v26, 16, v11
	v_fmac_f32_e32 v2, v10, v10
	v_and_b32_e32 v11, 0xffff0000, v11
	v_fmac_f32_e32 v2, v26, v26
	v_lshlrev_b32_e32 v27, 16, v12
	v_fmac_f32_e32 v2, v11, v11
	v_and_b32_e32 v12, 0xffff0000, v12
	v_fmac_f32_e32 v2, v27, v27
	v_lshlrev_b32_e32 v28, 16, v13
	v_fmac_f32_e32 v2, v12, v12
	v_and_b32_e32 v13, 0xffff0000, v13
	v_fmac_f32_e32 v2, v28, v28
	v_lshlrev_b32_e32 v29, 16, v14
	v_fmac_f32_e32 v2, v13, v13
	v_and_b32_e32 v14, 0xffff0000, v14
	v_fmac_f32_e32 v2, v29, v29
	v_lshlrev_b32_e32 v30, 16, v15
	v_fmac_f32_e32 v2, v14, v14
	v_and_b32_e32 v15, 0xffff0000, v15
	v_fmac_f32_e32 v2, v30, v30
	v_lshlrev_b32_e32 v31, 16, v16
	v_fmac_f32_e32 v2, v15, v15
	v_and_b32_e32 v16, 0xffff0000, v16
	v_fmac_f32_e32 v2, v31, v31
	v_lshlrev_b32_e32 v32, 16, v17
	v_fmac_f32_e32 v2, v16, v16
	v_and_b32_e32 v1, 0xffff0000, v17
	v_fmac_f32_e32 v2, v32, v32
	v_fmac_f32_e32 v2, v1, v1
	ds_bpermute_b32 v1, v76, v2
	s_waitcnt lgkmcnt(0)
	v_add_f32_e32 v1, v2, v1
	ds_bpermute_b32 v2, v77, v1
	s_waitcnt lgkmcnt(0)
	v_add_f32_e32 v1, v1, v2
	ds_bpermute_b32 v2, v78, v1
	s_waitcnt lgkmcnt(0)
	v_add_f32_e32 v1, v1, v2
	ds_bpermute_b32 v2, v79, v1
	s_waitcnt lgkmcnt(0)
	v_add_f32_e32 v1, v1, v2
	ds_bpermute_b32 v2, v80, v1
	s_waitcnt lgkmcnt(0)
	v_add_f32_e32 v2, v1, v2
	ds_bpermute_b32 v3, v81, v2
	s_and_saveexec_b64 s[36:37], s[2:3]
	s_cbranch_execz .LBB0_1883
	s_waitcnt lgkmcnt(0)
	v_add_f32_e32 v1, v2, v3
	v_fmamk_f32 v1, v1, 0x3a000000, v105
	v_mul_f32_e32 v2, 0x4f800000, v1
	v_cmp_gt_f32_e32 vcc, s81, v1
	s_nop 1
	v_cndmask_b32_e32 v1, v1, v2, vcc
	v_sqrt_f32_e32 v2, v1
	s_nop 0
	v_add_u32_e32 v3, -1, v2
	v_fma_f32 v5, -v3, v2, v1
	v_add_u32_e32 v4, 1, v2
	v_cmp_ge_f32_e64 s[34:35], 0, v5
	s_nop 1
	v_cndmask_b32_e64 v3, v2, v3, s[34:35]
	v_fma_f32 v2, -v4, v2, v1
	v_cmp_lt_f32_e64 s[34:35], 0, v2
	s_nop 1
	v_cndmask_b32_e64 v2, v3, v4, s[34:35]
	v_mul_f32_e32 v3, 0x37800000, v2
	v_cndmask_b32_e32 v2, v2, v3, vcc
	v_cmp_class_f32_e32 vcc, v1, v106
	s_nop 1
	v_cndmask_b32_e32 v1, v2, v1, vcc
	v_div_scale_f32 v2, s[34:35], v1, v1, 1.0
	v_rcp_f32_e32 v3, v2
	s_nop 0
	v_fma_f32 v4, -v2, v3, 1.0
	v_fmac_f32_e32 v3, v4, v3
	v_div_scale_f32 v4, vcc, 1.0, v1, 1.0
	v_mul_f32_e32 v5, v4, v3
	v_fma_f32 v6, -v2, v5, v4
	v_fmac_f32_e32 v5, v6, v3
	v_fma_f32 v2, -v2, v5, v4
	v_div_fmas_f32 v2, v2, v3, v5
	v_div_fixup_f32 v1, v2, v1, 1.0
	v_mov_b32_e32 v2, s68
	ds_write_b32 v2, v1 offset:12

.LBB0_1884:
	v_and_b32_e32 v62, 0xffffff00, v103
	v_lshl_add_u32 v63, v254, 2, v62
	v_lshlrev_b32_e32 v63, 2, v63
	global_load_dwordx4 v[200:203], v63, s[62:63]
	global_load_dwordx4 v[204:207], v63, s[34:35]
	global_load_dwordx4 v[208:211], v63, s[36:37]
	v_lshlrev_b32_e32 v64, 1, v103
	v_mov_b32_e32 v65, 0
	v_mov_b32_e32 v66, v103
	v_mov_b32_e32 v67, 0
	v_lshl_add_u64 v[196:197], v[48:49], 0, v[64:65]
	v_lshlrev_b32_e32 v68, 6, v62
	v_lshl_add_u32 v68, v254, 4, v68
	v_lshlrev_b32_e32 v69, 12, v75
	v_sub_u32_e32 v68, v68, v69
	v_ashrrev_i32_e32 v69, 31, v68
	v_lshl_add_u64 v[34:35], v[34:35], 0, v[68:69]
	v_lshl_add_u64 v[36:37], v[36:37], 0, v[68:69]
	v_lshl_add_u64 v[38:39], v[38:39], 0, v[68:69]
	v_lshl_add_u64 v[40:41], v[40:41], 0, v[68:69]
	v_mov_b32_e32 v198, 0x1000
	v_mov_b32_e32 v199, 0
	v_lshl_add_u64 v[72:73], v[50:51], 0, v[66:67]
	global_load_dwordx4 v[112:115], v[196:197], off
	global_load_dwordx4 v[116:119], v[34:35], off
	global_load_dwordx4 v[120:123], v[36:37], off
	global_load_dwordx4 v[124:127], v[38:39], off
	global_load_dwordx4 v[128:131], v[40:41], off
	global_load_dwordx4 v[132:135], v[196:197], off offset:32
	global_load_dwordx4 v[136:139], v[34:35], off offset:1024
	global_load_dwordx4 v[140:143], v[36:37], off offset:1024
	global_load_dwordx4 v[144:147], v[38:39], off offset:1024
	global_load_dwordx4 v[148:151], v[40:41], off offset:1024
	global_load_dwordx4 v[152:155], v[196:197], off offset:64
	global_load_dwordx4 v[156:159], v[34:35], off offset:2048
	global_load_dwordx4 v[160:163], v[36:37], off offset:2048
	global_load_dwordx4 v[164:167], v[38:39], off offset:2048
	global_load_dwordx4 v[168:171], v[40:41], off offset:2048
	global_load_dwordx4 v[172:175], v[196:197], off offset:96
	global_load_dwordx4 v[176:179], v[34:35], off offset:3072
	global_load_dwordx4 v[180:183], v[36:37], off offset:3072
	global_load_dwordx4 v[184:187], v[38:39], off offset:3072
	global_load_dwordx4 v[188:191], v[40:41], off offset:3072
	v_mul_u32_u24_e32 v62, 12, v62
	v_add_u32_e32 v62, 0x12000, v62
	v_lshl_add_u32 v1, v254, 4, v62
	v_and_b32_e32 v63, 8, v103
	v_lshl_add_u32 v111, v63, 2, v62
	s_waitcnt vmcnt(20)
	v_pk_add_f32 v[204:205], v[204:205], 1.0 op_sel_hi:[1,0]
	v_pk_add_f32 v[206:207], v[206:207], 1.0 op_sel_hi:[1,0]
	ds_write_b128 v1, v[200:203]
	ds_write_b128 v1, v[204:207] offset:1024
	ds_write_b128 v1, v[208:211] offset:2048
	s_waitcnt lgkmcnt(0)
	ds_read_b128 v[200:203], v111 offset:0
	ds_read_b128 v[204:207], v111 offset:16
	ds_read_b128 v[208:211], v111 offset:1024
	ds_read_b128 v[212:215], v111 offset:1040
	ds_read_b128 v[216:219], v111 offset:2048
	ds_read_b128 v[220:223], v111 offset:2064
	s_waitcnt lgkmcnt(0)
	ds_read_b128 v[224:227], v111 offset:64
	ds_read_b128 v[228:231], v111 offset:80
	ds_read_b128 v[232:235], v111 offset:1088
	ds_read_b128 v[236:239], v111 offset:1104
	ds_read_b128 v[240:243], v111 offset:2112
	ds_read_b128 v[244:247], v111 offset:2128
	s_waitcnt vmcnt(15)
	v_lshlrev_b32_e32 v54, 16, v112
	v_and_b32_e32 v55, 0xffff0000, v112
	v_lshlrev_b32_e32 v56, 16, v113
	v_and_b32_e32 v57, 0xffff0000, v113
	v_lshlrev_b32_e32 v58, 16, v114
	v_and_b32_e32 v59, 0xffff0000, v114
	v_lshlrev_b32_e32 v60, 16, v115
	v_and_b32_e32 v61, 0xffff0000, v115
	v_pk_mul_f32 v[54:55], v[46:47], v[54:55]
	v_pk_mul_f32 v[56:57], v[46:47], v[56:57]
	v_pk_mul_f32 v[58:59], v[46:47], v[58:59]
	v_pk_mul_f32 v[60:61], v[46:47], v[60:61]
	v_pk_mul_f32 v[54:55], v[200:201], v[54:55]
	v_pk_mul_f32 v[56:57], v[202:203], v[56:57]
	v_pk_mul_f32 v[58:59], v[204:205], v[58:59]
	v_pk_mul_f32 v[60:61], v[206:207], v[60:61]
	v_pk_fma_f32 v[54:55], v[208:209], v[54:55], v[216:217]
	v_pk_fma_f32 v[56:57], v[210:211], v[56:57], v[218:219]
	v_pk_fma_f32 v[58:59], v[212:213], v[58:59], v[220:221]
	v_pk_fma_f32 v[60:61], v[214:215], v[60:61], v[222:223]
	v_med3_f32 v62, v54, s82, v108
	v_med3_f32 v63, v55, s82, v108
	v_med3_f32 v64, v56, s82, v108
	v_med3_f32 v65, v57, s82, v108
	v_med3_f32 v66, v58, s82, v108
	v_med3_f32 v67, v59, s82, v108
	v_med3_f32 v68, v60, s82, v108
	v_med3_f32 v69, v61, s82, v108
	v_cvt_pk_bf16_f32 v192, v54, v55
	v_cvt_pk_bf16_f32 v193, v56, v57
	v_cvt_pk_bf16_f32 v194, v58, v59
	v_cvt_pk_bf16_f32 v195, v60, v61
	v_cvt_pk_fp8_f32 v70, v62, v63
	v_cvt_pk_fp8_f32 v71, v66, v67
	v_cvt_pk_fp8_f32 v70, v64, v65 op_sel:[0,0,1]
	v_cvt_pk_fp8_f32 v71, v68, v69 op_sel:[0,0,1]
	s_nop 0
	global_store_dwordx2 v[72:73], v[70:71], off
	v_mfma_f32_32x32x16_bf16 v[2:17], v[192:195], v[116:119], v[2:17]
	v_mfma_f32_32x32x16_bf16 v[18:33], v[192:195], v[120:123], v[18:33]
	v_mfma_f32_32x32x16_bf16 v[2:17], v[192:195], v[124:127], v[2:17]
	v_mfma_f32_32x32x16_bf16 v[18:33], v[192:195], v[128:131], v[18:33]
	v_lshlrev_b32_e32 v252, 16, v192
	v_and_b32_e32 v253, 0xffff0000, v192
	v_sub_f32_e32 v62, v54, v252
	v_sub_f32_e32 v63, v55, v253
	v_lshlrev_b32_e32 v252, 16, v193
	v_and_b32_e32 v253, 0xffff0000, v193
	v_sub_f32_e32 v64, v56, v252
	v_sub_f32_e32 v65, v57, v253
	v_lshlrev_b32_e32 v252, 16, v194
	v_and_b32_e32 v253, 0xffff0000, v194
	v_sub_f32_e32 v66, v58, v252
	v_sub_f32_e32 v67, v59, v253
	v_lshlrev_b32_e32 v252, 16, v195
	v_and_b32_e32 v253, 0xffff0000, v195
	v_sub_f32_e32 v68, v60, v252
	v_sub_f32_e32 v69, v61, v253
	v_cvt_pk_bf16_f32 v248, v62, v63
	v_cvt_pk_bf16_f32 v249, v64, v65
	v_cvt_pk_bf16_f32 v250, v66, v67
	v_cvt_pk_bf16_f32 v251, v68, v69
	s_nop 1
	v_mfma_f32_32x32x16_bf16 v[2:17], v[248:251], v[116:119], v[2:17]
	v_mfma_f32_32x32x16_bf16 v[18:33], v[248:251], v[120:123], v[18:33]
	global_load_dwordx4 v[112:115], v[196:197], off offset:128
	v_lshl_add_u64 v[34:35], v[34:35], 0, v[198:199]
	v_lshl_add_u64 v[36:37], v[36:37], 0, v[198:199]
	v_lshl_add_u64 v[38:39], v[38:39], 0, v[198:199]
	v_lshl_add_u64 v[40:41], v[40:41], 0, v[198:199]
	global_load_dwordx4 v[116:119], v[34:35], off
	global_load_dwordx4 v[120:123], v[36:37], off
	global_load_dwordx4 v[124:127], v[38:39], off
	global_load_dwordx4 v[128:131], v[40:41], off
	s_waitcnt lgkmcnt(0)
	ds_read_b128 v[200:203], v111 offset:128
	ds_read_b128 v[204:207], v111 offset:144
	ds_read_b128 v[208:211], v111 offset:1152
	ds_read_b128 v[212:215], v111 offset:1168
	ds_read_b128 v[216:219], v111 offset:2176
	ds_read_b128 v[220:223], v111 offset:2192
	s_waitcnt vmcnt(16)
	v_lshlrev_b32_e32 v54, 16, v132
	v_and_b32_e32 v55, 0xffff0000, v132
	v_lshlrev_b32_e32 v56, 16, v133
	v_and_b32_e32 v57, 0xffff0000, v133
	v_lshlrev_b32_e32 v58, 16, v134
	v_and_b32_e32 v59, 0xffff0000, v134
	v_lshlrev_b32_e32 v60, 16, v135
	v_and_b32_e32 v61, 0xffff0000, v135
	v_pk_mul_f32 v[54:55], v[46:47], v[54:55]
	v_pk_mul_f32 v[56:57], v[46:47], v[56:57]
	v_pk_mul_f32 v[58:59], v[46:47], v[58:59]
	v_pk_mul_f32 v[60:61], v[46:47], v[60:61]
	v_pk_mul_f32 v[54:55], v[224:225], v[54:55]
	v_pk_mul_f32 v[56:57], v[226:227], v[56:57]
	v_pk_mul_f32 v[58:59], v[228:229], v[58:59]
	v_pk_mul_f32 v[60:61], v[230:231], v[60:61]
	v_pk_fma_f32 v[54:55], v[232:233], v[54:55], v[240:241]
	v_pk_fma_f32 v[56:57], v[234:235], v[56:57], v[242:243]
	v_pk_fma_f32 v[58:59], v[236:237], v[58:59], v[244:245]
	v_pk_fma_f32 v[60:61], v[238:239], v[60:61], v[246:247]
	v_med3_f32 v62, v54, s82, v108
	v_med3_f32 v63, v55, s82, v108
	v_med3_f32 v64, v56, s82, v108
	v_med3_f32 v65, v57, s82, v108
	v_med3_f32 v66, v58, s82, v108
	v_med3_f32 v67, v59, s82, v108
	v_med3_f32 v68, v60, s82, v108
	v_med3_f32 v69, v61, s82, v108
	v_cvt_pk_bf16_f32 v192, v54, v55
	v_cvt_pk_bf16_f32 v193, v56, v57
	v_cvt_pk_bf16_f32 v194, v58, v59
	v_cvt_pk_bf16_f32 v195, v60, v61
	v_cvt_pk_fp8_f32 v70, v62, v63
	v_cvt_pk_fp8_f32 v71, v66, v67
	v_cvt_pk_fp8_f32 v70, v64, v65 op_sel:[0,0,1]
	v_cvt_pk_fp8_f32 v71, v68, v69 op_sel:[0,0,1]
	s_nop 0
	global_store_dwordx2 v[72:73], v[70:71], off offset:16
	v_mfma_f32_32x32x16_bf16 v[2:17], v[192:195], v[136:139], v[2:17]
	v_mfma_f32_32x32x16_bf16 v[18:33], v[192:195], v[140:143], v[18:33]
	v_mfma_f32_32x32x16_bf16 v[2:17], v[192:195], v[144:147], v[2:17]
	v_mfma_f32_32x32x16_bf16 v[18:33], v[192:195], v[148:151], v[18:33]
	v_lshlrev_b32_e32 v252, 16, v192
	v_and_b32_e32 v253, 0xffff0000, v192
	v_sub_f32_e32 v62, v54, v252
	v_sub_f32_e32 v63, v55, v253
	v_lshlrev_b32_e32 v252, 16, v193
	v_and_b32_e32 v253, 0xffff0000, v193
	v_sub_f32_e32 v64, v56, v252
	v_sub_f32_e32 v65, v57, v253
	v_lshlrev_b32_e32 v252, 16, v194
	v_and_b32_e32 v253, 0xffff0000, v194
	v_sub_f32_e32 v66, v58, v252
	v_sub_f32_e32 v67, v59, v253
	v_lshlrev_b32_e32 v252, 16, v195
	v_and_b32_e32 v253, 0xffff0000, v195
	v_sub_f32_e32 v68, v60, v252
	v_sub_f32_e32 v69, v61, v253
	v_cvt_pk_bf16_f32 v248, v62, v63
	v_cvt_pk_bf16_f32 v249, v64, v65
	v_cvt_pk_bf16_f32 v250, v66, v67
	v_cvt_pk_bf16_f32 v251, v68, v69
	s_nop 1
	v_mfma_f32_32x32x16_bf16 v[2:17], v[248:251], v[136:139], v[2:17]
	v_mfma_f32_32x32x16_bf16 v[18:33], v[248:251], v[140:143], v[18:33]
	global_load_dwordx4 v[132:135], v[196:197], off offset:160
	global_load_dwordx4 v[136:139], v[34:35], off offset:1024
	global_load_dwordx4 v[140:143], v[36:37], off offset:1024
	global_load_dwordx4 v[144:147], v[38:39], off offset:1024
	global_load_dwordx4 v[148:151], v[40:41], off offset:1024
	s_waitcnt lgkmcnt(0)
	ds_read_b128 v[224:227], v111 offset:192
	ds_read_b128 v[228:231], v111 offset:208
	ds_read_b128 v[232:235], v111 offset:1216
	ds_read_b128 v[236:239], v111 offset:1232
	ds_read_b128 v[240:243], v111 offset:2240
	ds_read_b128 v[244:247], v111 offset:2256
	s_waitcnt vmcnt(17)
	v_lshlrev_b32_e32 v54, 16, v152
	v_and_b32_e32 v55, 0xffff0000, v152
	v_lshlrev_b32_e32 v56, 16, v153
	v_and_b32_e32 v57, 0xffff0000, v153
	v_lshlrev_b32_e32 v58, 16, v154
	v_and_b32_e32 v59, 0xffff0000, v154
	v_lshlrev_b32_e32 v60, 16, v155
	v_and_b32_e32 v61, 0xffff0000, v155
	v_pk_mul_f32 v[54:55], v[46:47], v[54:55]
	v_pk_mul_f32 v[56:57], v[46:47], v[56:57]
	v_pk_mul_f32 v[58:59], v[46:47], v[58:59]
	v_pk_mul_f32 v[60:61], v[46:47], v[60:61]
	v_pk_mul_f32 v[54:55], v[200:201], v[54:55]
	v_pk_mul_f32 v[56:57], v[202:203], v[56:57]
	v_pk_mul_f32 v[58:59], v[204:205], v[58:59]
	v_pk_mul_f32 v[60:61], v[206:207], v[60:61]
	v_pk_fma_f32 v[54:55], v[208:209], v[54:55], v[216:217]
	v_pk_fma_f32 v[56:57], v[210:211], v[56:57], v[218:219]
	v_pk_fma_f32 v[58:59], v[212:213], v[58:59], v[220:221]
	v_pk_fma_f32 v[60:61], v[214:215], v[60:61], v[222:223]
	v_med3_f32 v62, v54, s82, v108
	v_med3_f32 v63, v55, s82, v108
	v_med3_f32 v64, v56, s82, v108
	v_med3_f32 v65, v57, s82, v108
	v_med3_f32 v66, v58, s82, v108
	v_med3_f32 v67, v59, s82, v108
	v_med3_f32 v68, v60, s82, v108
	v_med3_f32 v69, v61, s82, v108
	v_cvt_pk_bf16_f32 v192, v54, v55
	v_cvt_pk_bf16_f32 v193, v56, v57
	v_cvt_pk_bf16_f32 v194, v58, v59
	v_cvt_pk_bf16_f32 v195, v60, v61
	v_cvt_pk_fp8_f32 v70, v62, v63
	v_cvt_pk_fp8_f32 v71, v66, v67
	v_cvt_pk_fp8_f32 v70, v64, v65 op_sel:[0,0,1]
	v_cvt_pk_fp8_f32 v71, v68, v69 op_sel:[0,0,1]
	s_nop 0
	global_store_dwordx2 v[72:73], v[70:71], off offset:32
	v_mfma_f32_32x32x16_bf16 v[2:17], v[192:195], v[156:159], v[2:17]
	v_mfma_f32_32x32x16_bf16 v[18:33], v[192:195], v[160:163], v[18:33]
	v_mfma_f32_32x32x16_bf16 v[2:17], v[192:195], v[164:167], v[2:17]
	v_mfma_f32_32x32x16_bf16 v[18:33], v[192:195], v[168:171], v[18:33]
	v_lshlrev_b32_e32 v252, 16, v192
	v_and_b32_e32 v253, 0xffff0000, v192
	v_sub_f32_e32 v62, v54, v252
	v_sub_f32_e32 v63, v55, v253
	v_lshlrev_b32_e32 v252, 16, v193
	v_and_b32_e32 v253, 0xffff0000, v193
	v_sub_f32_e32 v64, v56, v252
	v_sub_f32_e32 v65, v57, v253
	v_lshlrev_b32_e32 v252, 16, v194
	v_and_b32_e32 v253, 0xffff0000, v194
	v_sub_f32_e32 v66, v58, v252
	v_sub_f32_e32 v67, v59, v253
	v_lshlrev_b32_e32 v252, 16, v195
	v_and_b32_e32 v253, 0xffff0000, v195
	v_sub_f32_e32 v68, v60, v252
	v_sub_f32_e32 v69, v61, v253
	v_cvt_pk_bf16_f32 v248, v62, v63
	v_cvt_pk_bf16_f32 v249, v64, v65
	v_cvt_pk_bf16_f32 v250, v66, v67
	v_cvt_pk_bf16_f32 v251, v68, v69
	s_nop 1
	v_mfma_f32_32x32x16_bf16 v[2:17], v[248:251], v[156:159], v[2:17]
	v_mfma_f32_32x32x16_bf16 v[18:33], v[248:251], v[160:163], v[18:33]
	global_load_dwordx4 v[152:155], v[196:197], off offset:192
	global_load_dwordx4 v[156:159], v[34:35], off offset:2048
	global_load_dwordx4 v[160:163], v[36:37], off offset:2048
	global_load_dwordx4 v[164:167], v[38:39], off offset:2048
	global_load_dwordx4 v[168:171], v[40:41], off offset:2048
	s_waitcnt lgkmcnt(0)
	ds_read_b128 v[200:203], v111 offset:256
	ds_read_b128 v[204:207], v111 offset:272
	ds_read_b128 v[208:211], v111 offset:1280
	ds_read_b128 v[212:215], v111 offset:1296
	ds_read_b128 v[216:219], v111 offset:2304
	ds_read_b128 v[220:223], v111 offset:2320
	s_waitcnt vmcnt(18)
	v_lshlrev_b32_e32 v54, 16, v172
	v_and_b32_e32 v55, 0xffff0000, v172
	v_lshlrev_b32_e32 v56, 16, v173
	v_and_b32_e32 v57, 0xffff0000, v173
	v_lshlrev_b32_e32 v58, 16, v174
	v_and_b32_e32 v59, 0xffff0000, v174
	v_lshlrev_b32_e32 v60, 16, v175
	v_and_b32_e32 v61, 0xffff0000, v175
	v_pk_mul_f32 v[54:55], v[46:47], v[54:55]
	v_pk_mul_f32 v[56:57], v[46:47], v[56:57]
	v_pk_mul_f32 v[58:59], v[46:47], v[58:59]
	v_pk_mul_f32 v[60:61], v[46:47], v[60:61]
	v_pk_mul_f32 v[54:55], v[224:225], v[54:55]
	v_pk_mul_f32 v[56:57], v[226:227], v[56:57]
	v_pk_mul_f32 v[58:59], v[228:229], v[58:59]
	v_pk_mul_f32 v[60:61], v[230:231], v[60:61]
	v_pk_fma_f32 v[54:55], v[232:233], v[54:55], v[240:241]
	v_pk_fma_f32 v[56:57], v[234:235], v[56:57], v[242:243]
	v_pk_fma_f32 v[58:59], v[236:237], v[58:59], v[244:245]
	v_pk_fma_f32 v[60:61], v[238:239], v[60:61], v[246:247]
	v_med3_f32 v62, v54, s82, v108
	v_med3_f32 v63, v55, s82, v108
	v_med3_f32 v64, v56, s82, v108
	v_med3_f32 v65, v57, s82, v108
	v_med3_f32 v66, v58, s82, v108
	v_med3_f32 v67, v59, s82, v108
	v_med3_f32 v68, v60, s82, v108
	v_med3_f32 v69, v61, s82, v108
	v_cvt_pk_bf16_f32 v192, v54, v55
	v_cvt_pk_bf16_f32 v193, v56, v57
	v_cvt_pk_bf16_f32 v194, v58, v59
	v_cvt_pk_bf16_f32 v195, v60, v61
	v_cvt_pk_fp8_f32 v70, v62, v63
	v_cvt_pk_fp8_f32 v71, v66, v67
	v_cvt_pk_fp8_f32 v70, v64, v65 op_sel:[0,0,1]
	v_cvt_pk_fp8_f32 v71, v68, v69 op_sel:[0,0,1]
	s_nop 0
	global_store_dwordx2 v[72:73], v[70:71], off offset:48
	v_mfma_f32_32x32x16_bf16 v[2:17], v[192:195], v[176:179], v[2:17]
	v_mfma_f32_32x32x16_bf16 v[18:33], v[192:195], v[180:183], v[18:33]
	v_mfma_f32_32x32x16_bf16 v[2:17], v[192:195], v[184:187], v[2:17]
	v_mfma_f32_32x32x16_bf16 v[18:33], v[192:195], v[188:191], v[18:33]
	v_lshlrev_b32_e32 v252, 16, v192
	v_and_b32_e32 v253, 0xffff0000, v192
	v_sub_f32_e32 v62, v54, v252
	v_sub_f32_e32 v63, v55, v253
	v_lshlrev_b32_e32 v252, 16, v193
	v_and_b32_e32 v253, 0xffff0000, v193
	v_sub_f32_e32 v64, v56, v252
	v_sub_f32_e32 v65, v57, v253
	v_lshlrev_b32_e32 v252, 16, v194
	v_and_b32_e32 v253, 0xffff0000, v194
	v_sub_f32_e32 v66, v58, v252
	v_sub_f32_e32 v67, v59, v253
	v_lshlrev_b32_e32 v252, 16, v195
	v_and_b32_e32 v253, 0xffff0000, v195
	v_sub_f32_e32 v68, v60, v252
	v_sub_f32_e32 v69, v61, v253
	v_cvt_pk_bf16_f32 v248, v62, v63
	v_cvt_pk_bf16_f32 v249, v64, v65
	v_cvt_pk_bf16_f32 v250, v66, v67
	v_cvt_pk_bf16_f32 v251, v68, v69
	s_nop 1
	v_mfma_f32_32x32x16_bf16 v[2:17], v[248:251], v[176:179], v[2:17]
	v_mfma_f32_32x32x16_bf16 v[18:33], v[248:251], v[180:183], v[18:33]
	global_load_dwordx4 v[172:175], v[196:197], off offset:224
	global_load_dwordx4 v[176:179], v[34:35], off offset:3072
	global_load_dwordx4 v[180:183], v[36:37], off offset:3072
	global_load_dwordx4 v[184:187], v[38:39], off offset:3072
	global_load_dwordx4 v[188:191], v[40:41], off offset:3072
	s_waitcnt lgkmcnt(0)
	ds_read_b128 v[224:227], v111 offset:320
	ds_read_b128 v[228:231], v111 offset:336
	ds_read_b128 v[232:235], v111 offset:1344
	ds_read_b128 v[236:239], v111 offset:1360
	ds_read_b128 v[240:243], v111 offset:2368
	ds_read_b128 v[244:247], v111 offset:2384
	s_waitcnt vmcnt(18)
	v_lshlrev_b32_e32 v54, 16, v112
	v_and_b32_e32 v55, 0xffff0000, v112
	v_lshlrev_b32_e32 v56, 16, v113
	v_and_b32_e32 v57, 0xffff0000, v113
	v_lshlrev_b32_e32 v58, 16, v114
	v_and_b32_e32 v59, 0xffff0000, v114
	v_lshlrev_b32_e32 v60, 16, v115
	v_and_b32_e32 v61, 0xffff0000, v115
	v_pk_mul_f32 v[54:55], v[46:47], v[54:55]
	v_pk_mul_f32 v[56:57], v[46:47], v[56:57]
	v_pk_mul_f32 v[58:59], v[46:47], v[58:59]
	v_pk_mul_f32 v[60:61], v[46:47], v[60:61]
	v_pk_mul_f32 v[54:55], v[200:201], v[54:55]
	v_pk_mul_f32 v[56:57], v[202:203], v[56:57]
	v_pk_mul_f32 v[58:59], v[204:205], v[58:59]
	v_pk_mul_f32 v[60:61], v[206:207], v[60:61]
	v_pk_fma_f32 v[54:55], v[208:209], v[54:55], v[216:217]
	v_pk_fma_f32 v[56:57], v[210:211], v[56:57], v[218:219]
	v_pk_fma_f32 v[58:59], v[212:213], v[58:59], v[220:221]
	v_pk_fma_f32 v[60:61], v[214:215], v[60:61], v[222:223]
	v_med3_f32 v62, v54, s82, v108
	v_med3_f32 v63, v55, s82, v108
	v_med3_f32 v64, v56, s82, v108
	v_med3_f32 v65, v57, s82, v108
	v_med3_f32 v66, v58, s82, v108
	v_med3_f32 v67, v59, s82, v108
	v_med3_f32 v68, v60, s82, v108
	v_med3_f32 v69, v61, s82, v108
	v_cvt_pk_bf16_f32 v192, v54, v55
	v_cvt_pk_bf16_f32 v193, v56, v57
	v_cvt_pk_bf16_f32 v194, v58, v59
	v_cvt_pk_bf16_f32 v195, v60, v61
	v_cvt_pk_fp8_f32 v70, v62, v63
	v_cvt_pk_fp8_f32 v71, v66, v67
	v_cvt_pk_fp8_f32 v70, v64, v65 op_sel:[0,0,1]
	v_cvt_pk_fp8_f32 v71, v68, v69 op_sel:[0,0,1]
	s_nop 0
	global_store_dwordx2 v[72:73], v[70:71], off offset:64
	v_mfma_f32_32x32x16_bf16 v[2:17], v[192:195], v[116:119], v[2:17]
	v_mfma_f32_32x32x16_bf16 v[18:33], v[192:195], v[120:123], v[18:33]
	v_mfma_f32_32x32x16_bf16 v[2:17], v[192:195], v[124:127], v[2:17]
	v_mfma_f32_32x32x16_bf16 v[18:33], v[192:195], v[128:131], v[18:33]
	v_lshlrev_b32_e32 v252, 16, v192
	v_and_b32_e32 v253, 0xffff0000, v192
	v_sub_f32_e32 v62, v54, v252
	v_sub_f32_e32 v63, v55, v253
	v_lshlrev_b32_e32 v252, 16, v193
	v_and_b32_e32 v253, 0xffff0000, v193
	v_sub_f32_e32 v64, v56, v252
	v_sub_f32_e32 v65, v57, v253
	v_lshlrev_b32_e32 v252, 16, v194
	v_and_b32_e32 v253, 0xffff0000, v194
	v_sub_f32_e32 v66, v58, v252
	v_sub_f32_e32 v67, v59, v253
	v_lshlrev_b32_e32 v252, 16, v195
	v_and_b32_e32 v253, 0xffff0000, v195
	v_sub_f32_e32 v68, v60, v252
	v_sub_f32_e32 v69, v61, v253
	v_cvt_pk_bf16_f32 v248, v62, v63
	v_cvt_pk_bf16_f32 v249, v64, v65
	v_cvt_pk_bf16_f32 v250, v66, v67
	v_cvt_pk_bf16_f32 v251, v68, v69
	s_nop 1
	v_mfma_f32_32x32x16_bf16 v[2:17], v[248:251], v[116:119], v[2:17]
	v_mfma_f32_32x32x16_bf16 v[18:33], v[248:251], v[120:123], v[18:33]
	global_load_dwordx4 v[112:115], v[196:197], off offset:256
	v_lshl_add_u64 v[34:35], v[34:35], 0, v[198:199]
	v_lshl_add_u64 v[36:37], v[36:37], 0, v[198:199]
	v_lshl_add_u64 v[38:39], v[38:39], 0, v[198:199]
	v_lshl_add_u64 v[40:41], v[40:41], 0, v[198:199]
	global_load_dwordx4 v[116:119], v[34:35], off
	global_load_dwordx4 v[120:123], v[36:37], off
	global_load_dwordx4 v[124:127], v[38:39], off
	global_load_dwordx4 v[128:131], v[40:41], off
	s_waitcnt lgkmcnt(0)
	ds_read_b128 v[200:203], v111 offset:384
	ds_read_b128 v[204:207], v111 offset:400
	ds_read_b128 v[208:211], v111 offset:1408
	ds_read_b128 v[212:215], v111 offset:1424
	ds_read_b128 v[216:219], v111 offset:2432
	ds_read_b128 v[220:223], v111 offset:2448
	s_waitcnt vmcnt(18)
	v_lshlrev_b32_e32 v54, 16, v132
	v_and_b32_e32 v55, 0xffff0000, v132
	v_lshlrev_b32_e32 v56, 16, v133
	v_and_b32_e32 v57, 0xffff0000, v133
	v_lshlrev_b32_e32 v58, 16, v134
	v_and_b32_e32 v59, 0xffff0000, v134
	v_lshlrev_b32_e32 v60, 16, v135
	v_and_b32_e32 v61, 0xffff0000, v135
	v_pk_mul_f32 v[54:55], v[46:47], v[54:55]
	v_pk_mul_f32 v[56:57], v[46:47], v[56:57]
	v_pk_mul_f32 v[58:59], v[46:47], v[58:59]
	v_pk_mul_f32 v[60:61], v[46:47], v[60:61]
	v_pk_mul_f32 v[54:55], v[224:225], v[54:55]
	v_pk_mul_f32 v[56:57], v[226:227], v[56:57]
	v_pk_mul_f32 v[58:59], v[228:229], v[58:59]
	v_pk_mul_f32 v[60:61], v[230:231], v[60:61]
	v_pk_fma_f32 v[54:55], v[232:233], v[54:55], v[240:241]
	v_pk_fma_f32 v[56:57], v[234:235], v[56:57], v[242:243]
	v_pk_fma_f32 v[58:59], v[236:237], v[58:59], v[244:245]
	v_pk_fma_f32 v[60:61], v[238:239], v[60:61], v[246:247]
	v_med3_f32 v62, v54, s82, v108
	v_med3_f32 v63, v55, s82, v108
	v_med3_f32 v64, v56, s82, v108
	v_med3_f32 v65, v57, s82, v108
	v_med3_f32 v66, v58, s82, v108
	v_med3_f32 v67, v59, s82, v108
	v_med3_f32 v68, v60, s82, v108
	v_med3_f32 v69, v61, s82, v108
	v_cvt_pk_bf16_f32 v192, v54, v55
	v_cvt_pk_bf16_f32 v193, v56, v57
	v_cvt_pk_bf16_f32 v194, v58, v59
	v_cvt_pk_bf16_f32 v195, v60, v61
	v_cvt_pk_fp8_f32 v70, v62, v63
	v_cvt_pk_fp8_f32 v71, v66, v67
	v_cvt_pk_fp8_f32 v70, v64, v65 op_sel:[0,0,1]
	v_cvt_pk_fp8_f32 v71, v68, v69 op_sel:[0,0,1]
	s_nop 0
	global_store_dwordx2 v[72:73], v[70:71], off offset:80
	v_mfma_f32_32x32x16_bf16 v[2:17], v[192:195], v[136:139], v[2:17]
	v_mfma_f32_32x32x16_bf16 v[18:33], v[192:195], v[140:143], v[18:33]
	v_mfma_f32_32x32x16_bf16 v[2:17], v[192:195], v[144:147], v[2:17]
	v_mfma_f32_32x32x16_bf16 v[18:33], v[192:195], v[148:151], v[18:33]
	v_lshlrev_b32_e32 v252, 16, v192
	v_and_b32_e32 v253, 0xffff0000, v192
	v_sub_f32_e32 v62, v54, v252
	v_sub_f32_e32 v63, v55, v253
	v_lshlrev_b32_e32 v252, 16, v193
	v_and_b32_e32 v253, 0xffff0000, v193
	v_sub_f32_e32 v64, v56, v252
	v_sub_f32_e32 v65, v57, v253
	v_lshlrev_b32_e32 v252, 16, v194
	v_and_b32_e32 v253, 0xffff0000, v194
	v_sub_f32_e32 v66, v58, v252
	v_sub_f32_e32 v67, v59, v253
	v_lshlrev_b32_e32 v252, 16, v195
	v_and_b32_e32 v253, 0xffff0000, v195
	v_sub_f32_e32 v68, v60, v252
	v_sub_f32_e32 v69, v61, v253
	v_cvt_pk_bf16_f32 v248, v62, v63
	v_cvt_pk_bf16_f32 v249, v64, v65
	v_cvt_pk_bf16_f32 v250, v66, v67
	v_cvt_pk_bf16_f32 v251, v68, v69
	s_nop 1
	v_mfma_f32_32x32x16_bf16 v[2:17], v[248:251], v[136:139], v[2:17]
	v_mfma_f32_32x32x16_bf16 v[18:33], v[248:251], v[140:143], v[18:33]
	global_load_dwordx4 v[132:135], v[196:197], off offset:288
	global_load_dwordx4 v[136:139], v[34:35], off offset:1024
	global_load_dwordx4 v[140:143], v[36:37], off offset:1024
	global_load_dwordx4 v[144:147], v[38:39], off offset:1024
	global_load_dwordx4 v[148:151], v[40:41], off offset:1024
	s_waitcnt lgkmcnt(0)
	ds_read_b128 v[224:227], v111 offset:448
	ds_read_b128 v[228:231], v111 offset:464
	ds_read_b128 v[232:235], v111 offset:1472
	ds_read_b128 v[236:239], v111 offset:1488
	ds_read_b128 v[240:243], v111 offset:2496
	ds_read_b128 v[244:247], v111 offset:2512
	s_waitcnt vmcnt(18)
	v_lshlrev_b32_e32 v54, 16, v152
	v_and_b32_e32 v55, 0xffff0000, v152
	v_lshlrev_b32_e32 v56, 16, v153
	v_and_b32_e32 v57, 0xffff0000, v153
	v_lshlrev_b32_e32 v58, 16, v154
	v_and_b32_e32 v59, 0xffff0000, v154
	v_lshlrev_b32_e32 v60, 16, v155
	v_and_b32_e32 v61, 0xffff0000, v155
	v_pk_mul_f32 v[54:55], v[46:47], v[54:55]
	v_pk_mul_f32 v[56:57], v[46:47], v[56:57]
	v_pk_mul_f32 v[58:59], v[46:47], v[58:59]
	v_pk_mul_f32 v[60:61], v[46:47], v[60:61]
	v_pk_mul_f32 v[54:55], v[200:201], v[54:55]
	v_pk_mul_f32 v[56:57], v[202:203], v[56:57]
	v_pk_mul_f32 v[58:59], v[204:205], v[58:59]
	v_pk_mul_f32 v[60:61], v[206:207], v[60:61]
	v_pk_fma_f32 v[54:55], v[208:209], v[54:55], v[216:217]
	v_pk_fma_f32 v[56:57], v[210:211], v[56:57], v[218:219]
	v_pk_fma_f32 v[58:59], v[212:213], v[58:59], v[220:221]
	v_pk_fma_f32 v[60:61], v[214:215], v[60:61], v[222:223]
	v_med3_f32 v62, v54, s82, v108
	v_med3_f32 v63, v55, s82, v108
	v_med3_f32 v64, v56, s82, v108
	v_med3_f32 v65, v57, s82, v108
	v_med3_f32 v66, v58, s82, v108
	v_med3_f32 v67, v59, s82, v108
	v_med3_f32 v68, v60, s82, v108
	v_med3_f32 v69, v61, s82, v108
	v_cvt_pk_bf16_f32 v192, v54, v55
	v_cvt_pk_bf16_f32 v193, v56, v57
	v_cvt_pk_bf16_f32 v194, v58, v59
	v_cvt_pk_bf16_f32 v195, v60, v61
	v_cvt_pk_fp8_f32 v70, v62, v63
	v_cvt_pk_fp8_f32 v71, v66, v67
	v_cvt_pk_fp8_f32 v70, v64, v65 op_sel:[0,0,1]
	v_cvt_pk_fp8_f32 v71, v68, v69 op_sel:[0,0,1]
	s_nop 0
	global_store_dwordx2 v[72:73], v[70:71], off offset:96
	v_mfma_f32_32x32x16_bf16 v[2:17], v[192:195], v[156:159], v[2:17]
	v_mfma_f32_32x32x16_bf16 v[18:33], v[192:195], v[160:163], v[18:33]
	v_mfma_f32_32x32x16_bf16 v[2:17], v[192:195], v[164:167], v[2:17]
	v_mfma_f32_32x32x16_bf16 v[18:33], v[192:195], v[168:171], v[18:33]
	v_lshlrev_b32_e32 v252, 16, v192
	v_and_b32_e32 v253, 0xffff0000, v192
	v_sub_f32_e32 v62, v54, v252
	v_sub_f32_e32 v63, v55, v253
	v_lshlrev_b32_e32 v252, 16, v193
	v_and_b32_e32 v253, 0xffff0000, v193
	v_sub_f32_e32 v64, v56, v252
	v_sub_f32_e32 v65, v57, v253
	v_lshlrev_b32_e32 v252, 16, v194
	v_and_b32_e32 v253, 0xffff0000, v194
	v_sub_f32_e32 v66, v58, v252
	v_sub_f32_e32 v67, v59, v253
	v_lshlrev_b32_e32 v252, 16, v195
	v_and_b32_e32 v253, 0xffff0000, v195
	v_sub_f32_e32 v68, v60, v252
	v_sub_f32_e32 v69, v61, v253
	v_cvt_pk_bf16_f32 v248, v62, v63
	v_cvt_pk_bf16_f32 v249, v64, v65
	v_cvt_pk_bf16_f32 v250, v66, v67
	v_cvt_pk_bf16_f32 v251, v68, v69
	s_nop 1
	v_mfma_f32_32x32x16_bf16 v[2:17], v[248:251], v[156:159], v[2:17]
	v_mfma_f32_32x32x16_bf16 v[18:33], v[248:251], v[160:163], v[18:33]
	global_load_dwordx4 v[152:155], v[196:197], off offset:320
	global_load_dwordx4 v[156:159], v[34:35], off offset:2048
	global_load_dwordx4 v[160:163], v[36:37], off offset:2048
	global_load_dwordx4 v[164:167], v[38:39], off offset:2048
	global_load_dwordx4 v[168:171], v[40:41], off offset:2048
	s_waitcnt lgkmcnt(0)
	ds_read_b128 v[200:203], v111 offset:512
	ds_read_b128 v[204:207], v111 offset:528
	ds_read_b128 v[208:211], v111 offset:1536
	ds_read_b128 v[212:215], v111 offset:1552
	ds_read_b128 v[216:219], v111 offset:2560
	ds_read_b128 v[220:223], v111 offset:2576
	s_waitcnt vmcnt(18)
	v_lshlrev_b32_e32 v54, 16, v172
	v_and_b32_e32 v55, 0xffff0000, v172
	v_lshlrev_b32_e32 v56, 16, v173
	v_and_b32_e32 v57, 0xffff0000, v173
	v_lshlrev_b32_e32 v58, 16, v174
	v_and_b32_e32 v59, 0xffff0000, v174
	v_lshlrev_b32_e32 v60, 16, v175
	v_and_b32_e32 v61, 0xffff0000, v175
	v_pk_mul_f32 v[54:55], v[46:47], v[54:55]
	v_pk_mul_f32 v[56:57], v[46:47], v[56:57]
	v_pk_mul_f32 v[58:59], v[46:47], v[58:59]
	v_pk_mul_f32 v[60:61], v[46:47], v[60:61]
	v_pk_mul_f32 v[54:55], v[224:225], v[54:55]
	v_pk_mul_f32 v[56:57], v[226:227], v[56:57]
	v_pk_mul_f32 v[58:59], v[228:229], v[58:59]
	v_pk_mul_f32 v[60:61], v[230:231], v[60:61]
	v_pk_fma_f32 v[54:55], v[232:233], v[54:55], v[240:241]
	v_pk_fma_f32 v[56:57], v[234:235], v[56:57], v[242:243]
	v_pk_fma_f32 v[58:59], v[236:237], v[58:59], v[244:245]
	v_pk_fma_f32 v[60:61], v[238:239], v[60:61], v[246:247]
	v_med3_f32 v62, v54, s82, v108
	v_med3_f32 v63, v55, s82, v108
	v_med3_f32 v64, v56, s82, v108
	v_med3_f32 v65, v57, s82, v108
	v_med3_f32 v66, v58, s82, v108
	v_med3_f32 v67, v59, s82, v108
	v_med3_f32 v68, v60, s82, v108
	v_med3_f32 v69, v61, s82, v108
	v_cvt_pk_bf16_f32 v192, v54, v55
	v_cvt_pk_bf16_f32 v193, v56, v57
	v_cvt_pk_bf16_f32 v194, v58, v59
	v_cvt_pk_bf16_f32 v195, v60, v61
	v_cvt_pk_fp8_f32 v70, v62, v63
	v_cvt_pk_fp8_f32 v71, v66, v67
	v_cvt_pk_fp8_f32 v70, v64, v65 op_sel:[0,0,1]
	v_cvt_pk_fp8_f32 v71, v68, v69 op_sel:[0,0,1]
	s_nop 0
	global_store_dwordx2 v[72:73], v[70:71], off offset:112
	v_mfma_f32_32x32x16_bf16 v[2:17], v[192:195], v[176:179], v[2:17]
	v_mfma_f32_32x32x16_bf16 v[18:33], v[192:195], v[180:183], v[18:33]
	v_mfma_f32_32x32x16_bf16 v[2:17], v[192:195], v[184:187], v[2:17]
	v_mfma_f32_32x32x16_bf16 v[18:33], v[192:195], v[188:191], v[18:33]
	v_lshlrev_b32_e32 v252, 16, v192
	v_and_b32_e32 v253, 0xffff0000, v192
	v_sub_f32_e32 v62, v54, v252
	v_sub_f32_e32 v63, v55, v253
	v_lshlrev_b32_e32 v252, 16, v193
	v_and_b32_e32 v253, 0xffff0000, v193
	v_sub_f32_e32 v64, v56, v252
	v_sub_f32_e32 v65, v57, v253
	v_lshlrev_b32_e32 v252, 16, v194
	v_and_b32_e32 v253, 0xffff0000, v194
	v_sub_f32_e32 v66, v58, v252
	v_sub_f32_e32 v67, v59, v253
	v_lshlrev_b32_e32 v252, 16, v195
	v_and_b32_e32 v253, 0xffff0000, v195
	v_sub_f32_e32 v68, v60, v252
	v_sub_f32_e32 v69, v61, v253
	v_cvt_pk_bf16_f32 v248, v62, v63
	v_cvt_pk_bf16_f32 v249, v64, v65
	v_cvt_pk_bf16_f32 v250, v66, v67
	v_cvt_pk_bf16_f32 v251, v68, v69
	s_nop 1
	v_mfma_f32_32x32x16_bf16 v[2:17], v[248:251], v[176:179], v[2:17]
	v_mfma_f32_32x32x16_bf16 v[18:33], v[248:251], v[180:183], v[18:33]
	global_load_dwordx4 v[172:175], v[196:197], off offset:352
	global_load_dwordx4 v[176:179], v[34:35], off offset:3072
	global_load_dwordx4 v[180:183], v[36:37], off offset:3072
	global_load_dwordx4 v[184:187], v[38:39], off offset:3072
	global_load_dwordx4 v[188:191], v[40:41], off offset:3072
	s_waitcnt lgkmcnt(0)
	ds_read_b128 v[224:227], v111 offset:576
	ds_read_b128 v[228:231], v111 offset:592
	ds_read_b128 v[232:235], v111 offset:1600
	ds_read_b128 v[236:239], v111 offset:1616
	ds_read_b128 v[240:243], v111 offset:2624
	ds_read_b128 v[244:247], v111 offset:2640
	s_waitcnt vmcnt(18)
	v_lshlrev_b32_e32 v54, 16, v112
	v_and_b32_e32 v55, 0xffff0000, v112
	v_lshlrev_b32_e32 v56, 16, v113
	v_and_b32_e32 v57, 0xffff0000, v113
	v_lshlrev_b32_e32 v58, 16, v114
	v_and_b32_e32 v59, 0xffff0000, v114
	v_lshlrev_b32_e32 v60, 16, v115
	v_and_b32_e32 v61, 0xffff0000, v115
	v_pk_mul_f32 v[54:55], v[46:47], v[54:55]
	v_pk_mul_f32 v[56:57], v[46:47], v[56:57]
	v_pk_mul_f32 v[58:59], v[46:47], v[58:59]
	v_pk_mul_f32 v[60:61], v[46:47], v[60:61]
	v_pk_mul_f32 v[54:55], v[200:201], v[54:55]
	v_pk_mul_f32 v[56:57], v[202:203], v[56:57]
	v_pk_mul_f32 v[58:59], v[204:205], v[58:59]
	v_pk_mul_f32 v[60:61], v[206:207], v[60:61]
	v_pk_fma_f32 v[54:55], v[208:209], v[54:55], v[216:217]
	v_pk_fma_f32 v[56:57], v[210:211], v[56:57], v[218:219]
	v_pk_fma_f32 v[58:59], v[212:213], v[58:59], v[220:221]
	v_pk_fma_f32 v[60:61], v[214:215], v[60:61], v[222:223]
	v_med3_f32 v62, v54, s82, v108
	v_med3_f32 v63, v55, s82, v108
	v_med3_f32 v64, v56, s82, v108
	v_med3_f32 v65, v57, s82, v108
	v_med3_f32 v66, v58, s82, v108
	v_med3_f32 v67, v59, s82, v108
	v_med3_f32 v68, v60, s82, v108
	v_med3_f32 v69, v61, s82, v108
	v_cvt_pk_bf16_f32 v192, v54, v55
	v_cvt_pk_bf16_f32 v193, v56, v57
	v_cvt_pk_bf16_f32 v194, v58, v59
	v_cvt_pk_bf16_f32 v195, v60, v61
	v_cvt_pk_fp8_f32 v70, v62, v63
	v_cvt_pk_fp8_f32 v71, v66, v67
	v_cvt_pk_fp8_f32 v70, v64, v65 op_sel:[0,0,1]
	v_cvt_pk_fp8_f32 v71, v68, v69 op_sel:[0,0,1]
	s_nop 0
	global_store_dwordx2 v[72:73], v[70:71], off offset:128
	v_mfma_f32_32x32x16_bf16 v[2:17], v[192:195], v[116:119], v[2:17]
	v_mfma_f32_32x32x16_bf16 v[18:33], v[192:195], v[120:123], v[18:33]
	v_mfma_f32_32x32x16_bf16 v[2:17], v[192:195], v[124:127], v[2:17]
	v_mfma_f32_32x32x16_bf16 v[18:33], v[192:195], v[128:131], v[18:33]
	v_lshlrev_b32_e32 v252, 16, v192
	v_and_b32_e32 v253, 0xffff0000, v192
	v_sub_f32_e32 v62, v54, v252
	v_sub_f32_e32 v63, v55, v253
	v_lshlrev_b32_e32 v252, 16, v193
	v_and_b32_e32 v253, 0xffff0000, v193
	v_sub_f32_e32 v64, v56, v252
	v_sub_f32_e32 v65, v57, v253
	v_lshlrev_b32_e32 v252, 16, v194
	v_and_b32_e32 v253, 0xffff0000, v194
	v_sub_f32_e32 v66, v58, v252
	v_sub_f32_e32 v67, v59, v253
	v_lshlrev_b32_e32 v252, 16, v195
	v_and_b32_e32 v253, 0xffff0000, v195
	v_sub_f32_e32 v68, v60, v252
	v_sub_f32_e32 v69, v61, v253
	v_cvt_pk_bf16_f32 v248, v62, v63
	v_cvt_pk_bf16_f32 v249, v64, v65
	v_cvt_pk_bf16_f32 v250, v66, v67
	v_cvt_pk_bf16_f32 v251, v68, v69
	s_nop 1
	v_mfma_f32_32x32x16_bf16 v[2:17], v[248:251], v[116:119], v[2:17]
	v_mfma_f32_32x32x16_bf16 v[18:33], v[248:251], v[120:123], v[18:33]
	global_load_dwordx4 v[112:115], v[196:197], off offset:384
	v_lshl_add_u64 v[34:35], v[34:35], 0, v[198:199]
	v_lshl_add_u64 v[36:37], v[36:37], 0, v[198:199]
	v_lshl_add_u64 v[38:39], v[38:39], 0, v[198:199]
	v_lshl_add_u64 v[40:41], v[40:41], 0, v[198:199]
	global_load_dwordx4 v[116:119], v[34:35], off
	global_load_dwordx4 v[120:123], v[36:37], off
	global_load_dwordx4 v[124:127], v[38:39], off
	global_load_dwordx4 v[128:131], v[40:41], off
	s_waitcnt lgkmcnt(0)
	ds_read_b128 v[200:203], v111 offset:640
	ds_read_b128 v[204:207], v111 offset:656
	ds_read_b128 v[208:211], v111 offset:1664
	ds_read_b128 v[212:215], v111 offset:1680
	ds_read_b128 v[216:219], v111 offset:2688
	ds_read_b128 v[220:223], v111 offset:2704
	s_waitcnt vmcnt(18)
	v_lshlrev_b32_e32 v54, 16, v132
	v_and_b32_e32 v55, 0xffff0000, v132
	v_lshlrev_b32_e32 v56, 16, v133
	v_and_b32_e32 v57, 0xffff0000, v133
	v_lshlrev_b32_e32 v58, 16, v134
	v_and_b32_e32 v59, 0xffff0000, v134
	v_lshlrev_b32_e32 v60, 16, v135
	v_and_b32_e32 v61, 0xffff0000, v135
	v_pk_mul_f32 v[54:55], v[46:47], v[54:55]
	v_pk_mul_f32 v[56:57], v[46:47], v[56:57]
	v_pk_mul_f32 v[58:59], v[46:47], v[58:59]
	v_pk_mul_f32 v[60:61], v[46:47], v[60:61]
	v_pk_mul_f32 v[54:55], v[224:225], v[54:55]
	v_pk_mul_f32 v[56:57], v[226:227], v[56:57]
	v_pk_mul_f32 v[58:59], v[228:229], v[58:59]
	v_pk_mul_f32 v[60:61], v[230:231], v[60:61]
	v_pk_fma_f32 v[54:55], v[232:233], v[54:55], v[240:241]
	v_pk_fma_f32 v[56:57], v[234:235], v[56:57], v[242:243]
	v_pk_fma_f32 v[58:59], v[236:237], v[58:59], v[244:245]
	v_pk_fma_f32 v[60:61], v[238:239], v[60:61], v[246:247]
	v_med3_f32 v62, v54, s82, v108
	v_med3_f32 v63, v55, s82, v108
	v_med3_f32 v64, v56, s82, v108
	v_med3_f32 v65, v57, s82, v108
	v_med3_f32 v66, v58, s82, v108
	v_med3_f32 v67, v59, s82, v108
	v_med3_f32 v68, v60, s82, v108
	v_med3_f32 v69, v61, s82, v108
	v_cvt_pk_bf16_f32 v192, v54, v55
	v_cvt_pk_bf16_f32 v193, v56, v57
	v_cvt_pk_bf16_f32 v194, v58, v59
	v_cvt_pk_bf16_f32 v195, v60, v61
	v_cvt_pk_fp8_f32 v70, v62, v63
	v_cvt_pk_fp8_f32 v71, v66, v67
	v_cvt_pk_fp8_f32 v70, v64, v65 op_sel:[0,0,1]
	v_cvt_pk_fp8_f32 v71, v68, v69 op_sel:[0,0,1]
	s_nop 0
	global_store_dwordx2 v[72:73], v[70:71], off offset:144
	v_mfma_f32_32x32x16_bf16 v[2:17], v[192:195], v[136:139], v[2:17]
	v_mfma_f32_32x32x16_bf16 v[18:33], v[192:195], v[140:143], v[18:33]
	v_mfma_f32_32x32x16_bf16 v[2:17], v[192:195], v[144:147], v[2:17]
	v_mfma_f32_32x32x16_bf16 v[18:33], v[192:195], v[148:151], v[18:33]
	v_lshlrev_b32_e32 v252, 16, v192
	v_and_b32_e32 v253, 0xffff0000, v192
	v_sub_f32_e32 v62, v54, v252
	v_sub_f32_e32 v63, v55, v253
	v_lshlrev_b32_e32 v252, 16, v193
	v_and_b32_e32 v253, 0xffff0000, v193
	v_sub_f32_e32 v64, v56, v252
	v_sub_f32_e32 v65, v57, v253
	v_lshlrev_b32_e32 v252, 16, v194
	v_and_b32_e32 v253, 0xffff0000, v194
	v_sub_f32_e32 v66, v58, v252
	v_sub_f32_e32 v67, v59, v253
	v_lshlrev_b32_e32 v252, 16, v195
	v_and_b32_e32 v253, 0xffff0000, v195
	v_sub_f32_e32 v68, v60, v252
	v_sub_f32_e32 v69, v61, v253
	v_cvt_pk_bf16_f32 v248, v62, v63
	v_cvt_pk_bf16_f32 v249, v64, v65
	v_cvt_pk_bf16_f32 v250, v66, v67
	v_cvt_pk_bf16_f32 v251, v68, v69
	s_nop 1
	v_mfma_f32_32x32x16_bf16 v[2:17], v[248:251], v[136:139], v[2:17]
	v_mfma_f32_32x32x16_bf16 v[18:33], v[248:251], v[140:143], v[18:33]
	global_load_dwordx4 v[132:135], v[196:197], off offset:416
	global_load_dwordx4 v[136:139], v[34:35], off offset:1024
	global_load_dwordx4 v[140:143], v[36:37], off offset:1024
	global_load_dwordx4 v[144:147], v[38:39], off offset:1024
	global_load_dwordx4 v[148:151], v[40:41], off offset:1024
	s_waitcnt lgkmcnt(0)
	ds_read_b128 v[224:227], v111 offset:704
	ds_read_b128 v[228:231], v111 offset:720
	ds_read_b128 v[232:235], v111 offset:1728
	ds_read_b128 v[236:239], v111 offset:1744
	ds_read_b128 v[240:243], v111 offset:2752
	ds_read_b128 v[244:247], v111 offset:2768
	s_waitcnt vmcnt(18)
	v_lshlrev_b32_e32 v54, 16, v152
	v_and_b32_e32 v55, 0xffff0000, v152
	v_lshlrev_b32_e32 v56, 16, v153
	v_and_b32_e32 v57, 0xffff0000, v153
	v_lshlrev_b32_e32 v58, 16, v154
	v_and_b32_e32 v59, 0xffff0000, v154
	v_lshlrev_b32_e32 v60, 16, v155
	v_and_b32_e32 v61, 0xffff0000, v155
	v_pk_mul_f32 v[54:55], v[46:47], v[54:55]
	v_pk_mul_f32 v[56:57], v[46:47], v[56:57]
	v_pk_mul_f32 v[58:59], v[46:47], v[58:59]
	v_pk_mul_f32 v[60:61], v[46:47], v[60:61]
	v_pk_mul_f32 v[54:55], v[200:201], v[54:55]
	v_pk_mul_f32 v[56:57], v[202:203], v[56:57]
	v_pk_mul_f32 v[58:59], v[204:205], v[58:59]
	v_pk_mul_f32 v[60:61], v[206:207], v[60:61]
	v_pk_fma_f32 v[54:55], v[208:209], v[54:55], v[216:217]
	v_pk_fma_f32 v[56:57], v[210:211], v[56:57], v[218:219]
	v_pk_fma_f32 v[58:59], v[212:213], v[58:59], v[220:221]
	v_pk_fma_f32 v[60:61], v[214:215], v[60:61], v[222:223]
	v_med3_f32 v62, v54, s82, v108
	v_med3_f32 v63, v55, s82, v108
	v_med3_f32 v64, v56, s82, v108
	v_med3_f32 v65, v57, s82, v108
	v_med3_f32 v66, v58, s82, v108
	v_med3_f32 v67, v59, s82, v108
	v_med3_f32 v68, v60, s82, v108
	v_med3_f32 v69, v61, s82, v108
	v_cvt_pk_bf16_f32 v192, v54, v55
	v_cvt_pk_bf16_f32 v193, v56, v57
	v_cvt_pk_bf16_f32 v194, v58, v59
	v_cvt_pk_bf16_f32 v195, v60, v61
	v_cvt_pk_fp8_f32 v70, v62, v63
	v_cvt_pk_fp8_f32 v71, v66, v67
	v_cvt_pk_fp8_f32 v70, v64, v65 op_sel:[0,0,1]
	v_cvt_pk_fp8_f32 v71, v68, v69 op_sel:[0,0,1]
	s_nop 0
	global_store_dwordx2 v[72:73], v[70:71], off offset:160
	v_mfma_f32_32x32x16_bf16 v[2:17], v[192:195], v[156:159], v[2:17]
	v_mfma_f32_32x32x16_bf16 v[18:33], v[192:195], v[160:163], v[18:33]
	v_mfma_f32_32x32x16_bf16 v[2:17], v[192:195], v[164:167], v[2:17]
	v_mfma_f32_32x32x16_bf16 v[18:33], v[192:195], v[168:171], v[18:33]
	v_lshlrev_b32_e32 v252, 16, v192
	v_and_b32_e32 v253, 0xffff0000, v192
	v_sub_f32_e32 v62, v54, v252
	v_sub_f32_e32 v63, v55, v253
	v_lshlrev_b32_e32 v252, 16, v193
	v_and_b32_e32 v253, 0xffff0000, v193
	v_sub_f32_e32 v64, v56, v252
	v_sub_f32_e32 v65, v57, v253
	v_lshlrev_b32_e32 v252, 16, v194
	v_and_b32_e32 v253, 0xffff0000, v194
	v_sub_f32_e32 v66, v58, v252
	v_sub_f32_e32 v67, v59, v253
	v_lshlrev_b32_e32 v252, 16, v195
	v_and_b32_e32 v253, 0xffff0000, v195
	v_sub_f32_e32 v68, v60, v252
	v_sub_f32_e32 v69, v61, v253
	v_cvt_pk_bf16_f32 v248, v62, v63
	v_cvt_pk_bf16_f32 v249, v64, v65
	v_cvt_pk_bf16_f32 v250, v66, v67
	v_cvt_pk_bf16_f32 v251, v68, v69
	s_nop 1
	v_mfma_f32_32x32x16_bf16 v[2:17], v[248:251], v[156:159], v[2:17]
	v_mfma_f32_32x32x16_bf16 v[18:33], v[248:251], v[160:163], v[18:33]
	global_load_dwordx4 v[152:155], v[196:197], off offset:448
	global_load_dwordx4 v[156:159], v[34:35], off offset:2048
	global_load_dwordx4 v[160:163], v[36:37], off offset:2048
	global_load_dwordx4 v[164:167], v[38:39], off offset:2048
	global_load_dwordx4 v[168:171], v[40:41], off offset:2048
	s_waitcnt lgkmcnt(0)
	ds_read_b128 v[200:203], v111 offset:768
	ds_read_b128 v[204:207], v111 offset:784
	ds_read_b128 v[208:211], v111 offset:1792
	ds_read_b128 v[212:215], v111 offset:1808
	ds_read_b128 v[216:219], v111 offset:2816
	ds_read_b128 v[220:223], v111 offset:2832
	s_waitcnt vmcnt(18)
	v_lshlrev_b32_e32 v54, 16, v172
	v_and_b32_e32 v55, 0xffff0000, v172
	v_lshlrev_b32_e32 v56, 16, v173
	v_and_b32_e32 v57, 0xffff0000, v173
	v_lshlrev_b32_e32 v58, 16, v174
	v_and_b32_e32 v59, 0xffff0000, v174
	v_lshlrev_b32_e32 v60, 16, v175
	v_and_b32_e32 v61, 0xffff0000, v175
	v_pk_mul_f32 v[54:55], v[46:47], v[54:55]
	v_pk_mul_f32 v[56:57], v[46:47], v[56:57]
	v_pk_mul_f32 v[58:59], v[46:47], v[58:59]
	v_pk_mul_f32 v[60:61], v[46:47], v[60:61]
	v_pk_mul_f32 v[54:55], v[224:225], v[54:55]
	v_pk_mul_f32 v[56:57], v[226:227], v[56:57]
	v_pk_mul_f32 v[58:59], v[228:229], v[58:59]
	v_pk_mul_f32 v[60:61], v[230:231], v[60:61]
	v_pk_fma_f32 v[54:55], v[232:233], v[54:55], v[240:241]
	v_pk_fma_f32 v[56:57], v[234:235], v[56:57], v[242:243]
	v_pk_fma_f32 v[58:59], v[236:237], v[58:59], v[244:245]
	v_pk_fma_f32 v[60:61], v[238:239], v[60:61], v[246:247]
	v_med3_f32 v62, v54, s82, v108
	v_med3_f32 v63, v55, s82, v108
	v_med3_f32 v64, v56, s82, v108
	v_med3_f32 v65, v57, s82, v108
	v_med3_f32 v66, v58, s82, v108
	v_med3_f32 v67, v59, s82, v108
	v_med3_f32 v68, v60, s82, v108
	v_med3_f32 v69, v61, s82, v108
	v_cvt_pk_bf16_f32 v192, v54, v55
	v_cvt_pk_bf16_f32 v193, v56, v57
	v_cvt_pk_bf16_f32 v194, v58, v59
	v_cvt_pk_bf16_f32 v195, v60, v61
	v_cvt_pk_fp8_f32 v70, v62, v63
	v_cvt_pk_fp8_f32 v71, v66, v67
	v_cvt_pk_fp8_f32 v70, v64, v65 op_sel:[0,0,1]
	v_cvt_pk_fp8_f32 v71, v68, v69 op_sel:[0,0,1]
	s_nop 0
	global_store_dwordx2 v[72:73], v[70:71], off offset:176
	v_mfma_f32_32x32x16_bf16 v[2:17], v[192:195], v[176:179], v[2:17]
	v_mfma_f32_32x32x16_bf16 v[18:33], v[192:195], v[180:183], v[18:33]
	v_mfma_f32_32x32x16_bf16 v[2:17], v[192:195], v[184:187], v[2:17]
	v_mfma_f32_32x32x16_bf16 v[18:33], v[192:195], v[188:191], v[18:33]
	v_lshlrev_b32_e32 v252, 16, v192
	v_and_b32_e32 v253, 0xffff0000, v192
	v_sub_f32_e32 v62, v54, v252
	v_sub_f32_e32 v63, v55, v253
	v_lshlrev_b32_e32 v252, 16, v193
	v_and_b32_e32 v253, 0xffff0000, v193
	v_sub_f32_e32 v64, v56, v252
	v_sub_f32_e32 v65, v57, v253
	v_lshlrev_b32_e32 v252, 16, v194
	v_and_b32_e32 v253, 0xffff0000, v194
	v_sub_f32_e32 v66, v58, v252
	v_sub_f32_e32 v67, v59, v253
	v_lshlrev_b32_e32 v252, 16, v195
	v_and_b32_e32 v253, 0xffff0000, v195
	v_sub_f32_e32 v68, v60, v252
	v_sub_f32_e32 v69, v61, v253
	v_cvt_pk_bf16_f32 v248, v62, v63
	v_cvt_pk_bf16_f32 v249, v64, v65
	v_cvt_pk_bf16_f32 v250, v66, v67
	v_cvt_pk_bf16_f32 v251, v68, v69
	s_nop 1
	v_mfma_f32_32x32x16_bf16 v[2:17], v[248:251], v[176:179], v[2:17]
	v_mfma_f32_32x32x16_bf16 v[18:33], v[248:251], v[180:183], v[18:33]
	global_load_dwordx4 v[172:175], v[196:197], off offset:480
	global_load_dwordx4 v[176:179], v[34:35], off offset:3072
	global_load_dwordx4 v[180:183], v[36:37], off offset:3072
	global_load_dwordx4 v[184:187], v[38:39], off offset:3072
	global_load_dwordx4 v[188:191], v[40:41], off offset:3072
	s_waitcnt lgkmcnt(0)
	ds_read_b128 v[224:227], v111 offset:832
	ds_read_b128 v[228:231], v111 offset:848
	ds_read_b128 v[232:235], v111 offset:1856
	ds_read_b128 v[236:239], v111 offset:1872
	ds_read_b128 v[240:243], v111 offset:2880
	ds_read_b128 v[244:247], v111 offset:2896
	s_waitcnt vmcnt(18)
	v_lshlrev_b32_e32 v54, 16, v112
	v_and_b32_e32 v55, 0xffff0000, v112
	v_lshlrev_b32_e32 v56, 16, v113
	v_and_b32_e32 v57, 0xffff0000, v113
	v_lshlrev_b32_e32 v58, 16, v114
	v_and_b32_e32 v59, 0xffff0000, v114
	v_lshlrev_b32_e32 v60, 16, v115
	v_and_b32_e32 v61, 0xffff0000, v115
	v_pk_mul_f32 v[54:55], v[46:47], v[54:55]
	v_pk_mul_f32 v[56:57], v[46:47], v[56:57]
	v_pk_mul_f32 v[58:59], v[46:47], v[58:59]
	v_pk_mul_f32 v[60:61], v[46:47], v[60:61]
	v_pk_mul_f32 v[54:55], v[200:201], v[54:55]
	v_pk_mul_f32 v[56:57], v[202:203], v[56:57]
	v_pk_mul_f32 v[58:59], v[204:205], v[58:59]
	v_pk_mul_f32 v[60:61], v[206:207], v[60:61]
	v_pk_fma_f32 v[54:55], v[208:209], v[54:55], v[216:217]
	v_pk_fma_f32 v[56:57], v[210:211], v[56:57], v[218:219]
	v_pk_fma_f32 v[58:59], v[212:213], v[58:59], v[220:221]
	v_pk_fma_f32 v[60:61], v[214:215], v[60:61], v[222:223]
	v_med3_f32 v62, v54, s82, v108
	v_med3_f32 v63, v55, s82, v108
	v_med3_f32 v64, v56, s82, v108
	v_med3_f32 v65, v57, s82, v108
	v_med3_f32 v66, v58, s82, v108
	v_med3_f32 v67, v59, s82, v108
	v_med3_f32 v68, v60, s82, v108
	v_med3_f32 v69, v61, s82, v108
	v_cvt_pk_bf16_f32 v192, v54, v55
	v_cvt_pk_bf16_f32 v193, v56, v57
	v_cvt_pk_bf16_f32 v194, v58, v59
	v_cvt_pk_bf16_f32 v195, v60, v61
	v_cvt_pk_fp8_f32 v70, v62, v63
	v_cvt_pk_fp8_f32 v71, v66, v67
	v_cvt_pk_fp8_f32 v70, v64, v65 op_sel:[0,0,1]
	v_cvt_pk_fp8_f32 v71, v68, v69 op_sel:[0,0,1]
	s_nop 0
	global_store_dwordx2 v[72:73], v[70:71], off offset:192
	v_mfma_f32_32x32x16_bf16 v[2:17], v[192:195], v[116:119], v[2:17]
	v_mfma_f32_32x32x16_bf16 v[18:33], v[192:195], v[120:123], v[18:33]
	v_mfma_f32_32x32x16_bf16 v[2:17], v[192:195], v[124:127], v[2:17]
	v_mfma_f32_32x32x16_bf16 v[18:33], v[192:195], v[128:131], v[18:33]
	v_lshlrev_b32_e32 v252, 16, v192
	v_and_b32_e32 v253, 0xffff0000, v192
	v_sub_f32_e32 v62, v54, v252
	v_sub_f32_e32 v63, v55, v253
	v_lshlrev_b32_e32 v252, 16, v193
	v_and_b32_e32 v253, 0xffff0000, v193
	v_sub_f32_e32 v64, v56, v252
	v_sub_f32_e32 v65, v57, v253
	v_lshlrev_b32_e32 v252, 16, v194
	v_and_b32_e32 v253, 0xffff0000, v194
	v_sub_f32_e32 v66, v58, v252
	v_sub_f32_e32 v67, v59, v253
	v_lshlrev_b32_e32 v252, 16, v195
	v_and_b32_e32 v253, 0xffff0000, v195
	v_sub_f32_e32 v68, v60, v252
	v_sub_f32_e32 v69, v61, v253
	v_cvt_pk_bf16_f32 v248, v62, v63
	v_cvt_pk_bf16_f32 v249, v64, v65
	v_cvt_pk_bf16_f32 v250, v66, v67
	v_cvt_pk_bf16_f32 v251, v68, v69
	s_nop 1
	v_mfma_f32_32x32x16_bf16 v[2:17], v[248:251], v[116:119], v[2:17]
	v_mfma_f32_32x32x16_bf16 v[18:33], v[248:251], v[120:123], v[18:33]
	s_waitcnt lgkmcnt(0)
	ds_read_b128 v[200:203], v111 offset:896
	ds_read_b128 v[204:207], v111 offset:912
	ds_read_b128 v[208:211], v111 offset:1920
	ds_read_b128 v[212:215], v111 offset:1936
	ds_read_b128 v[216:219], v111 offset:2944
	ds_read_b128 v[220:223], v111 offset:2960
	s_waitcnt vmcnt(13)
	v_lshlrev_b32_e32 v54, 16, v132
	v_and_b32_e32 v55, 0xffff0000, v132
	v_lshlrev_b32_e32 v56, 16, v133
	v_and_b32_e32 v57, 0xffff0000, v133
	v_lshlrev_b32_e32 v58, 16, v134
	v_and_b32_e32 v59, 0xffff0000, v134
	v_lshlrev_b32_e32 v60, 16, v135
	v_and_b32_e32 v61, 0xffff0000, v135
	v_pk_mul_f32 v[54:55], v[46:47], v[54:55]
	v_pk_mul_f32 v[56:57], v[46:47], v[56:57]
	v_pk_mul_f32 v[58:59], v[46:47], v[58:59]
	v_pk_mul_f32 v[60:61], v[46:47], v[60:61]
	v_pk_mul_f32 v[54:55], v[224:225], v[54:55]
	v_pk_mul_f32 v[56:57], v[226:227], v[56:57]
	v_pk_mul_f32 v[58:59], v[228:229], v[58:59]
	v_pk_mul_f32 v[60:61], v[230:231], v[60:61]
	v_pk_fma_f32 v[54:55], v[232:233], v[54:55], v[240:241]
	v_pk_fma_f32 v[56:57], v[234:235], v[56:57], v[242:243]
	v_pk_fma_f32 v[58:59], v[236:237], v[58:59], v[244:245]
	v_pk_fma_f32 v[60:61], v[238:239], v[60:61], v[246:247]
	v_med3_f32 v62, v54, s82, v108
	v_med3_f32 v63, v55, s82, v108
	v_med3_f32 v64, v56, s82, v108
	v_med3_f32 v65, v57, s82, v108
	v_med3_f32 v66, v58, s82, v108
	v_med3_f32 v67, v59, s82, v108
	v_med3_f32 v68, v60, s82, v108
	v_med3_f32 v69, v61, s82, v108
	v_cvt_pk_bf16_f32 v192, v54, v55
	v_cvt_pk_bf16_f32 v193, v56, v57
	v_cvt_pk_bf16_f32 v194, v58, v59
	v_cvt_pk_bf16_f32 v195, v60, v61
	v_cvt_pk_fp8_f32 v70, v62, v63
	v_cvt_pk_fp8_f32 v71, v66, v67
	v_cvt_pk_fp8_f32 v70, v64, v65 op_sel:[0,0,1]
	v_cvt_pk_fp8_f32 v71, v68, v69 op_sel:[0,0,1]
	s_nop 0
	global_store_dwordx2 v[72:73], v[70:71], off offset:208
	v_mfma_f32_32x32x16_bf16 v[2:17], v[192:195], v[136:139], v[2:17]
	v_mfma_f32_32x32x16_bf16 v[18:33], v[192:195], v[140:143], v[18:33]
	v_mfma_f32_32x32x16_bf16 v[2:17], v[192:195], v[144:147], v[2:17]
	v_mfma_f32_32x32x16_bf16 v[18:33], v[192:195], v[148:151], v[18:33]
	v_lshlrev_b32_e32 v252, 16, v192
	v_and_b32_e32 v253, 0xffff0000, v192
	v_sub_f32_e32 v62, v54, v252
	v_sub_f32_e32 v63, v55, v253
	v_lshlrev_b32_e32 v252, 16, v193
	v_and_b32_e32 v253, 0xffff0000, v193
	v_sub_f32_e32 v64, v56, v252
	v_sub_f32_e32 v65, v57, v253
	v_lshlrev_b32_e32 v252, 16, v194
	v_and_b32_e32 v253, 0xffff0000, v194
	v_sub_f32_e32 v66, v58, v252
	v_sub_f32_e32 v67, v59, v253
	v_lshlrev_b32_e32 v252, 16, v195
	v_and_b32_e32 v253, 0xffff0000, v195
	v_sub_f32_e32 v68, v60, v252
	v_sub_f32_e32 v69, v61, v253
	v_cvt_pk_bf16_f32 v248, v62, v63
	v_cvt_pk_bf16_f32 v249, v64, v65
	v_cvt_pk_bf16_f32 v250, v66, v67
	v_cvt_pk_bf16_f32 v251, v68, v69
	s_nop 1
	v_mfma_f32_32x32x16_bf16 v[2:17], v[248:251], v[136:139], v[2:17]
	v_mfma_f32_32x32x16_bf16 v[18:33], v[248:251], v[140:143], v[18:33]
	s_waitcnt lgkmcnt(0)
	ds_read_b128 v[224:227], v111 offset:960
	ds_read_b128 v[228:231], v111 offset:976
	ds_read_b128 v[232:235], v111 offset:1984
	ds_read_b128 v[236:239], v111 offset:2000
	ds_read_b128 v[240:243], v111 offset:3008
	ds_read_b128 v[244:247], v111 offset:3024
	s_waitcnt vmcnt(8)
	v_lshlrev_b32_e32 v54, 16, v152
	v_and_b32_e32 v55, 0xffff0000, v152
	v_lshlrev_b32_e32 v56, 16, v153
	v_and_b32_e32 v57, 0xffff0000, v153
	v_lshlrev_b32_e32 v58, 16, v154
	v_and_b32_e32 v59, 0xffff0000, v154
	v_lshlrev_b32_e32 v60, 16, v155
	v_and_b32_e32 v61, 0xffff0000, v155
	v_pk_mul_f32 v[54:55], v[46:47], v[54:55]
	v_pk_mul_f32 v[56:57], v[46:47], v[56:57]
	v_pk_mul_f32 v[58:59], v[46:47], v[58:59]
	v_pk_mul_f32 v[60:61], v[46:47], v[60:61]
	v_pk_mul_f32 v[54:55], v[200:201], v[54:55]
	v_pk_mul_f32 v[56:57], v[202:203], v[56:57]
	v_pk_mul_f32 v[58:59], v[204:205], v[58:59]
	v_pk_mul_f32 v[60:61], v[206:207], v[60:61]
	v_pk_fma_f32 v[54:55], v[208:209], v[54:55], v[216:217]
	v_pk_fma_f32 v[56:57], v[210:211], v[56:57], v[218:219]
	v_pk_fma_f32 v[58:59], v[212:213], v[58:59], v[220:221]
	v_pk_fma_f32 v[60:61], v[214:215], v[60:61], v[222:223]
	v_med3_f32 v62, v54, s82, v108
	v_med3_f32 v63, v55, s82, v108
	v_med3_f32 v64, v56, s82, v108
	v_med3_f32 v65, v57, s82, v108
	v_med3_f32 v66, v58, s82, v108
	v_med3_f32 v67, v59, s82, v108
	v_med3_f32 v68, v60, s82, v108
	v_med3_f32 v69, v61, s82, v108
	v_cvt_pk_bf16_f32 v192, v54, v55
	v_cvt_pk_bf16_f32 v193, v56, v57
	v_cvt_pk_bf16_f32 v194, v58, v59
	v_cvt_pk_bf16_f32 v195, v60, v61
	v_cvt_pk_fp8_f32 v70, v62, v63
	v_cvt_pk_fp8_f32 v71, v66, v67
	v_cvt_pk_fp8_f32 v70, v64, v65 op_sel:[0,0,1]
	v_cvt_pk_fp8_f32 v71, v68, v69 op_sel:[0,0,1]
	s_nop 0
	global_store_dwordx2 v[72:73], v[70:71], off offset:224
	v_mfma_f32_32x32x16_bf16 v[2:17], v[192:195], v[156:159], v[2:17]
	v_mfma_f32_32x32x16_bf16 v[18:33], v[192:195], v[160:163], v[18:33]
	v_mfma_f32_32x32x16_bf16 v[2:17], v[192:195], v[164:167], v[2:17]
	v_mfma_f32_32x32x16_bf16 v[18:33], v[192:195], v[168:171], v[18:33]
	v_lshlrev_b32_e32 v252, 16, v192
	v_and_b32_e32 v253, 0xffff0000, v192
	v_sub_f32_e32 v62, v54, v252
	v_sub_f32_e32 v63, v55, v253
	v_lshlrev_b32_e32 v252, 16, v193
	v_and_b32_e32 v253, 0xffff0000, v193
	v_sub_f32_e32 v64, v56, v252
	v_sub_f32_e32 v65, v57, v253
	v_lshlrev_b32_e32 v252, 16, v194
	v_and_b32_e32 v253, 0xffff0000, v194
	v_sub_f32_e32 v66, v58, v252
	v_sub_f32_e32 v67, v59, v253
	v_lshlrev_b32_e32 v252, 16, v195
	v_and_b32_e32 v253, 0xffff0000, v195
	v_sub_f32_e32 v68, v60, v252
	v_sub_f32_e32 v69, v61, v253
	v_cvt_pk_bf16_f32 v248, v62, v63
	v_cvt_pk_bf16_f32 v249, v64, v65
	v_cvt_pk_bf16_f32 v250, v66, v67
	v_cvt_pk_bf16_f32 v251, v68, v69
	s_nop 1
	v_mfma_f32_32x32x16_bf16 v[2:17], v[248:251], v[156:159], v[2:17]
	v_mfma_f32_32x32x16_bf16 v[18:33], v[248:251], v[160:163], v[18:33]
	s_waitcnt lgkmcnt(0)
	s_waitcnt vmcnt(3)
	v_lshlrev_b32_e32 v54, 16, v172
	v_and_b32_e32 v55, 0xffff0000, v172
	v_lshlrev_b32_e32 v56, 16, v173
	v_and_b32_e32 v57, 0xffff0000, v173
	v_lshlrev_b32_e32 v58, 16, v174
	v_and_b32_e32 v59, 0xffff0000, v174
	v_lshlrev_b32_e32 v60, 16, v175
	v_and_b32_e32 v61, 0xffff0000, v175
	v_pk_mul_f32 v[54:55], v[46:47], v[54:55]
	v_pk_mul_f32 v[56:57], v[46:47], v[56:57]
	v_pk_mul_f32 v[58:59], v[46:47], v[58:59]
	v_pk_mul_f32 v[60:61], v[46:47], v[60:61]
	v_pk_mul_f32 v[54:55], v[224:225], v[54:55]
	v_pk_mul_f32 v[56:57], v[226:227], v[56:57]
	v_pk_mul_f32 v[58:59], v[228:229], v[58:59]
	v_pk_mul_f32 v[60:61], v[230:231], v[60:61]
	v_pk_fma_f32 v[54:55], v[232:233], v[54:55], v[240:241]
	v_pk_fma_f32 v[56:57], v[234:235], v[56:57], v[242:243]
	v_pk_fma_f32 v[58:59], v[236:237], v[58:59], v[244:245]
	v_pk_fma_f32 v[60:61], v[238:239], v[60:61], v[246:247]
	v_med3_f32 v62, v54, s82, v108
	v_med3_f32 v63, v55, s82, v108
	v_med3_f32 v64, v56, s82, v108
	v_med3_f32 v65, v57, s82, v108
	v_med3_f32 v66, v58, s82, v108
	v_med3_f32 v67, v59, s82, v108
	v_med3_f32 v68, v60, s82, v108
	v_med3_f32 v69, v61, s82, v108
	v_cvt_pk_bf16_f32 v192, v54, v55
	v_cvt_pk_bf16_f32 v193, v56, v57
	v_cvt_pk_bf16_f32 v194, v58, v59
	v_cvt_pk_bf16_f32 v195, v60, v61
	v_cvt_pk_fp8_f32 v70, v62, v63
	v_cvt_pk_fp8_f32 v71, v66, v67
	v_cvt_pk_fp8_f32 v70, v64, v65 op_sel:[0,0,1]
	v_cvt_pk_fp8_f32 v71, v68, v69 op_sel:[0,0,1]
	s_nop 0
	global_store_dwordx2 v[72:73], v[70:71], off offset:240
	v_mfma_f32_32x32x16_bf16 v[2:17], v[192:195], v[176:179], v[2:17]
	v_mfma_f32_32x32x16_bf16 v[18:33], v[192:195], v[180:183], v[18:33]
	v_mfma_f32_32x32x16_bf16 v[2:17], v[192:195], v[184:187], v[2:17]
	v_mfma_f32_32x32x16_bf16 v[18:33], v[192:195], v[188:191], v[18:33]
	v_lshlrev_b32_e32 v252, 16, v192
	v_and_b32_e32 v253, 0xffff0000, v192
	v_sub_f32_e32 v62, v54, v252
	v_sub_f32_e32 v63, v55, v253
	v_lshlrev_b32_e32 v252, 16, v193
	v_and_b32_e32 v253, 0xffff0000, v193
	v_sub_f32_e32 v64, v56, v252
	v_sub_f32_e32 v65, v57, v253
	v_lshlrev_b32_e32 v252, 16, v194
	v_and_b32_e32 v253, 0xffff0000, v194
	v_sub_f32_e32 v66, v58, v252
	v_sub_f32_e32 v67, v59, v253
	v_lshlrev_b32_e32 v252, 16, v195
	v_and_b32_e32 v253, 0xffff0000, v195
	v_sub_f32_e32 v68, v60, v252
	v_sub_f32_e32 v69, v61, v253
	v_cvt_pk_bf16_f32 v248, v62, v63
	v_cvt_pk_bf16_f32 v249, v64, v65
	v_cvt_pk_bf16_f32 v250, v66, v67
	v_cvt_pk_bf16_f32 v251, v68, v69
	s_nop 1
	v_mfma_f32_32x32x16_bf16 v[2:17], v[248:251], v[176:179], v[2:17]
	v_mfma_f32_32x32x16_bf16 v[18:33], v[248:251], v[180:183], v[18:33]
	v_and_b32_e32 v62, 0xffffff00, v103
	v_lshlrev_b32_e32 v62, 6, v62
	v_lshl_add_u32 v62, v254, 4, v62
	v_lshlrev_b32_e32 v63, 12, v75
	v_sub_u32_e32 v62, v62, v63
	v_add_u32_e32 v62, 0x3000, v62
	v_sub_u32_e32 v62, 0, v62
	v_ashrrev_i32_e32 v63, 31, v62
	v_lshl_add_u64 v[34:35], v[34:35], 0, v[62:63]
	v_lshl_add_u64 v[36:37], v[36:37], 0, v[62:63]
	v_lshl_add_u64 v[38:39], v[38:39], 0, v[62:63]
	v_lshl_add_u64 v[40:41], v[40:41], 0, v[62:63]
	s_nop 7
	v_add_u32_e32 v1, 0x400, v83
	s_nop 9
	ds_write2_b32 v1, v2, v18 offset1:32
	ds_write2_b32 v1, v3, v19 offset0:64 offset1:96
	ds_write2_b32 v1, v4, v20 offset0:128 offset1:160
	ds_write2_b32 v1, v5, v21 offset0:192 offset1:224
	v_add_u32_e32 v1, 0xc00, v83
	ds_write2_b32 v1, v6, v22 offset1:32
	ds_write2_b32 v1, v7, v23 offset0:64 offset1:96
	ds_write2_b32 v1, v8, v24 offset0:128 offset1:160
	ds_write2_b32 v1, v9, v25 offset0:192 offset1:224
	v_add_u32_e32 v1, 0x1400, v83
	ds_write2_b32 v1, v10, v26 offset1:32
	ds_write2_b32 v1, v11, v27 offset0:64 offset1:96
	ds_write2_b32 v1, v12, v28 offset0:128 offset1:160
	ds_write2_b32 v1, v13, v29 offset0:192 offset1:224
	v_add_u32_e32 v1, 0x1c00, v83
	ds_write2_b32 v1, v14, v30 offset1:32
	ds_write2_b32 v1, v15, v31 offset0:64 offset1:96
	ds_write2_b32 v1, v16, v32 offset0:128 offset1:160
	ds_write2_b32 v1, v17, v33 offset0:192 offset1:224
	s_waitcnt lgkmcnt(0)
	s_barrier
	global_load_dword v1, v[42:43], off
	v_add_u32_e32 v8, s66, v84
	ds_read2st64_b32 v[2:3], v8 offset0:4 offset1:36
	ds_read2st64_b32 v[4:5], v8 offset0:68 offset1:100
	ds_read2st64_b32 v[6:7], v8 offset0:132 offset1:164
	ds_read2st64_b32 v[8:9], v8 offset0:196 offset1:228
	s_waitcnt lgkmcnt(3)
	v_add_f32_e32 v2, 0, v2
	v_add_f32_e32 v2, v2, v3
	s_waitcnt lgkmcnt(2)
	v_add_f32_e32 v2, v2, v4
	v_add_f32_e32 v2, v2, v5
	s_waitcnt lgkmcnt(1)
	v_add_f32_e32 v2, v2, v6
	v_add_f32_e32 v2, v2, v7
	s_waitcnt lgkmcnt(0)
	v_add_f32_e32 v2, v2, v8
	v_add_f32_e32 v2, v2, v9
	v_mul_f32_e32 v3, 0xbfb8aa3b, v2
	v_fma_f32 v4, v2, s83, -v3
	v_rndne_f32_e32 v5, v3
	v_fmac_f32_e32 v4, 0xb2a5705f, v2
	v_sub_f32_e32 v3, v3, v5
	v_add_f32_e32 v3, v3, v4
	v_cvt_i32_f32_e32 v5, v5
	v_exp_f32_e32 v3, v3
	v_cmp_nlt_f32_e32 vcc, s84, v2
	v_ldexp_f32 v3, v3, v5
	s_nop 0
	v_cndmask_b32_e32 v3, 0, v3, vcc
	v_cmp_ngt_f32_e32 vcc, s85, v2
	s_nop 1
	v_cndmask_b32_e32 v2, v109, v3, vcc
	v_add_f32_e32 v2, 1.0, v2
	v_div_scale_f32 v3, s[34:35], v2, v2, 1.0
	v_rcp_f32_e32 v4, v3
	v_div_scale_f32 v5, vcc, 1.0, v2, 1.0
	v_fma_f32 v6, -v3, v4, 1.0
	v_fmac_f32_e32 v4, v6, v4
	v_mul_f32_e32 v6, v5, v4
	v_fma_f32 v7, -v3, v6, v5
	v_fmac_f32_e32 v6, v7, v4
	v_fma_f32 v3, -v3, v6, v5
	v_div_fmas_f32 v3, v3, v4, v6
	v_div_fixup_f32 v2, v3, v2, 1.0
	s_waitcnt vmcnt(0)
	v_add_f32_e32 v1, v1, v2
	ds_bpermute_b32 v3, v88, v1
	ds_bpermute_b32 v4, v89, v1
	ds_bpermute_b32 v5, v90, v1
	ds_bpermute_b32 v6, v91, v1
	ds_bpermute_b32 v7, v92, v1
	s_waitcnt lgkmcnt(4)
	v_cmp_eq_f32_e64 s[34:35], v1, v3
	v_cmp_lt_f32_e32 vcc, v1, v3
	s_waitcnt lgkmcnt(3)
	v_cmp_eq_f32_e64 s[38:39], v1, v4
	s_and_b64 s[34:35], s[4:5], s[34:35]
	v_cmp_lt_f32_e64 s[36:37], v1, v4
	s_waitcnt lgkmcnt(2)
	v_cmp_eq_f32_e64 s[42:43], v1, v5
	s_and_b64 s[38:39], s[6:7], s[38:39]
	s_or_b64 s[34:35], vcc, s[34:35]
	v_cmp_lt_f32_e64 s[40:41], v1, v5
	s_waitcnt lgkmcnt(1)
	v_cmp_eq_f32_e64 s[46:47], v1, v6
	s_and_b64 s[42:43], s[8:9], s[42:43]
	v_cndmask_b32_e64 v3, 0, 1, s[34:35]
	s_or_b64 s[34:35], s[36:37], s[38:39]
	v_cmp_lt_f32_e64 s[44:45], v1, v6
	s_and_b64 s[46:47], s[10:11], s[46:47]
	v_cndmask_b32_e64 v4, 0, 1, s[34:35]
	s_or_b64 s[34:35], s[40:41], s[42:43]
	v_cndmask_b32_e64 v5, 0, 1, s[34:35]
	s_or_b64 s[34:35], s[44:45], s[46:47]
	v_add3_u32 v3, v3, v4, v5
	v_cndmask_b32_e64 v4, 0, 1, s[34:35]
	s_waitcnt lgkmcnt(0)
	v_cmp_eq_f32_e64 s[34:35], v1, v7
	v_cmp_lt_f32_e32 vcc, v1, v7
	ds_bpermute_b32 v5, v93, v1
	s_and_b64 s[34:35], s[12:13], s[34:35]
	s_or_b64 s[34:35], vcc, s[34:35]
	v_cndmask_b32_e64 v6, 0, 1, s[34:35]
	v_add3_u32 v3, v3, v4, v6
	ds_bpermute_b32 v4, v94, v1
	s_waitcnt lgkmcnt(1)
	v_cmp_eq_f32_e64 s[34:35], v1, v5
	ds_bpermute_b32 v6, v95, v1
	v_cmp_lt_f32_e32 vcc, v1, v5
	s_and_b64 s[34:35], s[14:15], s[34:35]
	s_or_b64 s[34:35], vcc, s[34:35]
	v_cndmask_b32_e64 v5, 0, 1, s[34:35]
	s_waitcnt lgkmcnt(1)
	v_cmp_eq_f32_e64 s[34:35], v1, v4
	v_cmp_lt_f32_e32 vcc, v1, v4
	s_and_b64 s[34:35], s[16:17], s[34:35]
	s_or_b64 s[34:35], vcc, s[34:35]
	s_waitcnt lgkmcnt(0)
	v_cmp_lt_f32_e32 vcc, v1, v6
	v_cndmask_b32_e64 v4, 0, 1, s[34:35]
	s_mov_b32 s40, 0
	v_addc_co_u32_e32 v3, vcc, v3, v5, vcc
	v_add_u32_e32 v3, v3, v4
	v_cmp_gt_u32_e32 vcc, 2, v3
	s_nop 1
	v_cndmask_b32_e32 v3, 0, v1, vcc
	ds_bpermute_b32 v4, v76, v3
	s_waitcnt lgkmcnt(0)
	v_add_f32_e32 v3, v3, v4
	ds_bpermute_b32 v4, v77, v3
	s_waitcnt lgkmcnt(0)
	v_add_f32_e32 v3, v3, v4
	ds_bpermute_b32 v4, v78, v3
	s_waitcnt lgkmcnt(0)
	v_add_f32_e32 v3, v3, v4
	ds_bpermute_b32 v4, v87, v3
	ds_bpermute_b32 v5, v96, v3
	ds_bpermute_b32 v6, v97, v3
	ds_bpermute_b32 v7, v98, v3
	ds_bpermute_b32 v8, v99, v3
	s_waitcnt lgkmcnt(4)
	v_cmp_eq_f32_e64 s[34:35], v3, v4
	v_cmp_lt_f32_e32 vcc, v3, v4
	s_and_b64 s[34:35], s[18:19], s[34:35]
	s_or_b64 s[34:35], vcc, s[34:35]
	v_cndmask_b32_e64 v4, 0, 1, s[34:35]
	s_waitcnt lgkmcnt(3)
	v_cmp_eq_f32_e64 s[34:35], v3, v5
	v_cmp_lt_f32_e32 vcc, v3, v5
	s_and_b64 s[34:35], s[20:21], s[34:35]
	s_or_b64 s[34:35], vcc, s[34:35]
	v_cndmask_b32_e64 v5, 0, 1, s[34:35]
	s_waitcnt lgkmcnt(2)
	v_cmp_eq_f32_e64 s[34:35], v3, v6
	v_cmp_lt_f32_e32 vcc, v3, v6
	s_and_b64 s[34:35], s[22:23], s[34:35]
	s_or_b64 s[34:35], vcc, s[34:35]
	v_cndmask_b32_e64 v6, 0, 1, s[34:35]
	s_waitcnt lgkmcnt(1)
	v_cmp_eq_f32_e64 s[34:35], v3, v7
	v_cmp_lt_f32_e32 vcc, v3, v7
	s_and_b64 s[34:35], s[24:25], s[34:35]
	ds_bpermute_b32 v9, v100, v3
	s_or_b64 s[34:35], vcc, s[34:35]
	v_cndmask_b32_e64 v7, 0, 1, s[34:35]
	s_waitcnt lgkmcnt(1)
	v_cmp_eq_f32_e64 s[34:35], v3, v8
	v_cmp_lt_f32_e32 vcc, v3, v8
	s_and_b64 s[34:35], s[26:27], s[34:35]
	ds_bpermute_b32 v10, v101, v3
	s_or_b64 s[34:35], vcc, s[34:35]
	v_cndmask_b32_e64 v8, 0, 1, s[34:35]
	s_waitcnt lgkmcnt(1)
	v_cmp_eq_f32_e64 s[34:35], v3, v9
	ds_bpermute_b32 v11, v102, v3
	v_cmp_lt_f32_e32 vcc, v3, v9
	s_and_b64 s[34:35], s[28:29], s[34:35]
	s_or_b64 s[34:35], vcc, s[34:35]
	v_cndmask_b32_e64 v9, 0, 1, s[34:35]
	s_waitcnt lgkmcnt(1)
	v_cmp_eq_f32_e64 s[34:35], v3, v10
	v_cmp_lt_f32_e32 vcc, v3, v10
	s_and_b64 s[34:35], s[30:31], s[34:35]
	s_or_b64 s[34:35], vcc, s[34:35]
	s_waitcnt lgkmcnt(0)
	v_cmp_lt_f32_e32 vcc, v3, v11
	v_cndmask_b32_e64 v10, 0, 1, s[34:35]
	s_nop 0
	v_cndmask_b32_e64 v3, 0, 1, vcc
	v_add_u32_e32 v3, v5, v3
	v_add3_u32 v3, v3, v4, v6
	v_add3_u32 v3, v3, v7, v8
	v_add3_u32 v3, v3, v9, v10
	v_cmp_gt_u32_e32 vcc, 4, v3
	v_mov_b32_e32 v5, 0
	v_mov_b32_e32 v4, v104
	v_cndmask_b32_e32 v3, v110, v1, vcc
